# rider split: GQA units keep expert-weight tiles 0..11, differential units convert tiles 12..23
# speedup vs baseline: 1.0166x; 1.0127x over previous
; DI f32x16 mfma8(v8i a, v8i b, f32x16 c) { return __builtin_amdgcn_mfma_scale_f32_32x32x64_f8f6f4(a, b, c, 0, 0, 0, 0, 0, 0); }
; DI void attn_unit_d8(unsigned char* lds, const AttnArgs& a) {
;     ...
;     auto tile = [&](const unsigned char* Kb, const unsigned char* Kn, v8i& Pa, v8i& Pb, v8i& v0, v8i& v1, const v8i& Qa, const v8i& Qb, const v8i& w0, const v8i& w1) __attribute__((always_inline)) {
;         qk(Kb, 1, s1a, s1b);
;         v0 = rd32(Kb + voff); v1 = rd32(Kb + voff + 32 * A8_PITCH);
;         o0[0] = mfma8(w0, Qa, o0[0]); o1[0] = mfma8(w0, Qb, o1[0]); o0[1] = mfma8(w1, Qa, o0[1]); o1[1] = mfma8(w1, Qb, o1[1]);
;         expsum(s0a, l0); expsum(s0b, l1); pack4(s0a, Pa, 0); pack4(s0b, Pb, 0);
;         qk(Kn, 0, s0a, s0b);
;         expsum(s1a, l0); expsum(s1b, l1); pack4(s1a, Pa, 4); pack4(s1b, Pb, 4);
; #pragma unroll
;         for (int i = 0; i < 8; ++i) { __builtin_amdgcn_sched_group_barrier(0x008, 1, 0); __builtin_amdgcn_sched_group_barrier(0x402, 22, 0); }
;     };
;     for (int t = a.t0; t < a.t1; t += 2) {
;         const int s1 = sb + 1 >= 5 ? sb - 4 : sb + 1, s2 = sb + 2 >= 5 ? sb - 3 : sb + 2, s3 = sb + 3 >= 5 ? sb - 2 : sb + 3, s4 = sb + 4 >= 5 ? sb - 1 : sb + 4;
;         { const int ta = t + 3, tb = t + 4; gload(ta < a.t1 ? ta : a.t1 - 1, kreg0, vreg0); gload(tb < a.t1 ? tb : a.t1 - 1, kreg1, vreg1); }
;         tile(lds + sb * D8_SLOT, lds + s1 * D8_SLOT, PaX, PbX, vX0, vX1, PaY, PbY, vY0, vY1);
;         tile(lds + s1 * D8_SLOT, lds + s2 * D8_SLOT, PaY, PbY, vY0, vY1, PaX, PbX, vX0, vX1);
;         lstore(s3, kreg0, vreg0); lstore(s4, kreg1, vreg1);
;         __syncthreads();
;         sb = s2;
;     }
.LBB0_663:
	s_cmp_gt_i32 s16, 3
	s_cselect_b32 s17, -4, 1
	s_add_i32 s18, s17, s16
	s_mul_i32 s6, s16, 0x2800
	s_cmp_gt_i32 s16, 2
	v_mfma_f32_32x32x64_f8f6f4 v[50:65], v[154:161], v[138:145], v[50:65]
	v_exp_f32_e32 v192, v90
	v_add_u32_e32 v90, s6, v218
	s_cselect_b32 s6, -3, 2
	s_add_i32 s6, s6, s16
	s_cmp_gt_i32 s16, 1
	s_cselect_b32 s19, -2, 3
	s_add_i32 s19, s19, s16
	s_cmp_gt_i32 s16, 0
	s_cselect_b32 s49, -1, 4
	s_min_u32 s54, s46, 64
	s_add_i32 s49, s49, s16
	s_cmp_lt_u32 s46, 61
	s_mul_i32 s17, s6, 0x2800
	s_mov_b32 s16, s6
	s_cselect_b64 s[52:53], -1, 0
	s_lshl_b32 s6, s54, 6
	s_add_i32 s54, s6, 0xc0
	s_add_i32 s55, s6, 0xfffff0c0
	s_and_b64 s[52:53], s[52:53], exec
	v_lshl_add_u64 v[98:99], v[182:183], 0, s[6:7]
	s_cselect_b32 s6, s54, s55
	s_cselect_b32 s53, s21, s48
	s_cselect_b32 s52, s20, s47
	s_min_u32 s56, s46, 63
	v_exp_f32_e32 v198, v82
	v_exp_f32_e32 v199, v83
	v_exp_f32_e32 v196, v84
	v_exp_f32_e32 v197, v85
	v_exp_f32_e32 v200, v86
	v_exp_f32_e32 v201, v87
	v_exp_f32_e32 v194, v88
	v_exp_f32_e32 v195, v89
	ds_read_b128 v[82:85], v90 offset:2560
	ds_read_b128 v[86:89], v90 offset:2576
	global_load_dwordx2 v[202:203], v[98:99], off offset:192
	v_add_u32_e32 v98, s6, v215
	s_cmp_lt_u32 s46, 60
	v_ashrrev_i32_e32 v99, 31, v98
	s_cselect_b64 s[54:55], -1, 0
	s_lshl_b32 s6, s56, 6
	v_lshlrev_b64 v[98:99], 8, v[98:99]
	s_add_i32 s56, s6, 0x100
	s_add_i32 s57, s6, 0xfffff100
	v_lshl_add_u64 v[98:99], s[52:53], 0, v[98:99]
	s_and_b64 s[52:53], s[54:55], exec
	s_cselect_b32 s54, s56, s57
	v_lshl_add_u64 v[220:221], v[98:99], 0, v[178:179]
	v_add_u32_e32 v98, s54, v215
	v_ashrrev_i32_e32 v99, 31, v98
	s_cselect_b32 s53, s21, s48
	s_cselect_b32 s52, s20, s47
	v_lshlrev_b64 v[98:99], 8, v[98:99]
	v_lshl_add_u64 v[100:101], v[182:183], 0, s[6:7]
	v_lshl_add_u64 v[98:99], s[52:53], 0, v[98:99]
	global_load_dwordx2 v[204:205], v[100:101], off offset:256
	v_lshl_add_u64 v[222:223], v[98:99], 0, v[178:179]
	s_waitcnt lgkmcnt(0)
	v_mfma_f32_32x32x64_f8f6f4 v[98:113], v[82:89], v[114:121], 0
	v_exp_f32_e32 v193, v91
	v_exp_f32_e32 v224, v92
	v_exp_f32_e32 v225, v93
	v_exp_f32_e32 v226, v94
	v_exp_f32_e32 v227, v95
	v_exp_f32_e32 v228, v96
	v_exp_f32_e32 v229, v97
	ds_read_b128 v[170:173], v90 offset:5120
	ds_read_b128 v[174:177], v90 offset:5136
	ds_read_b128 v[162:165], v90 offset:7680
	ds_read_b128 v[166:169], v90 offset:7696
	v_pk_add_f32 v[90:91], v[186:187], v[198:199]
	v_pk_add_f32 v[92:93], v[184:185], v[196:197]
	v_pk_add_f32 v[90:91], v[200:201], v[90:91]
	v_pk_add_f32 v[92:93], v[194:195], v[92:93]
	v_pk_add_f32 v[90:91], v[192:193], v[90:91]
	v_pk_add_f32 v[92:93], v[224:225], v[92:93]
	v_exp_f32_e32 v66, v66
	v_exp_f32_e32 v67, v67
	v_exp_f32_e32 v68, v68
	v_exp_f32_e32 v69, v69
	v_exp_f32_e32 v70, v70
	v_exp_f32_e32 v71, v71
	v_exp_f32_e32 v72, v72
	v_pk_add_f32 v[230:231], v[228:229], v[92:93]
	v_pk_add_f32 v[232:233], v[226:227], v[90:91]
	v_mfma_f32_32x32x64_f8f6f4 v[82:97], v[82:89], v[122:129], 0
	v_exp_f32_e32 v73, v73
	v_exp_f32_e32 v74, v74
	v_exp_f32_e32 v75, v75
	v_exp_f32_e32 v76, v76
	v_exp_f32_e32 v77, v77
	v_exp_f32_e32 v78, v78
	v_exp_f32_e32 v79, v79
	v_exp_f32_e32 v80, v80
	v_exp_f32_e32 v81, v81
	v_pk_add_f32 v[186:187], v[190:191], v[66:67]
	v_pk_add_f32 v[188:189], v[188:189], v[68:69]
	s_nop 0
	v_pk_add_f32 v[186:187], v[70:71], v[186:187]
	v_pk_add_f32 v[188:189], v[72:73], v[188:189]
	s_nop 0
	v_cvt_scalef32_pk_fp8_f32 v184, v198, v199, s36
	v_pk_add_f32 v[186:187], v[74:75], v[186:187]
	v_pk_add_f32 v[188:189], v[76:77], v[188:189]
	v_cvt_scalef32_pk_fp8_f32 v185, v200, v201, s36
	v_cvt_scalef32_pk_fp8_f32 v184, v196, v197, s36 op_sel:[0,0,0,1]
	v_pk_add_f32 v[190:191], v[78:79], v[186:187]
	v_pk_add_f32 v[188:189], v[80:81], v[188:189]
	v_mfma_f32_32x32x64_f8f6f4 v[2:17], v[154:161], v[130:137], v[2:17]
	s_nop 0
	s_nop 0
	s_nop 0
	s_nop 0
	s_nop 0
	s_nop 0
	s_mulk_i32 s18, 0x2800
	v_cvt_scalef32_pk_fp8_f32 v186, v192, v193, s36
	v_cvt_scalef32_pk_fp8_f32 v187, v226, v227, s36
	v_cvt_scalef32_pk_fp8_f32 v154, v66, v67, s36
	v_cvt_scalef32_pk_fp8_f32 v155, v70, v71, s36
	v_cvt_scalef32_pk_fp8_f32 v156, v74, v75, s36
	v_cvt_scalef32_pk_fp8_f32 v157, v78, v79, s36
	v_cvt_scalef32_pk_fp8_f32 v185, v194, v195, s36 op_sel:[0,0,0,1]
	v_add_u32_e32 v219, s18, v218
	v_cvt_scalef32_pk_fp8_f32 v186, v224, v225, s36 op_sel:[0,0,0,1]
	v_cvt_scalef32_pk_fp8_f32 v187, v228, v229, s36 op_sel:[0,0,0,1]
	v_cvt_scalef32_pk_fp8_f32 v154, v68, v69, s36 op_sel:[0,0,0,1]
	v_cvt_scalef32_pk_fp8_f32 v155, v72, v73, s36 op_sel:[0,0,0,1]
	v_cvt_scalef32_pk_fp8_f32 v156, v76, v77, s36 op_sel:[0,0,0,1]
	v_cvt_scalef32_pk_fp8_f32 v157, v80, v81, s36 op_sel:[0,0,0,1]
	v_exp_f32_e32 v98, v98
	v_exp_f32_e32 v99, v99
	v_mfma_f32_32x32x64_f8f6f4 v[34:49], v[146:153], v[138:145], v[34:49]
	v_exp_f32_e32 v100, v100
	v_exp_f32_e32 v101, v101
	v_exp_f32_e32 v102, v102
	v_exp_f32_e32 v103, v103
	v_exp_f32_e32 v104, v104
	v_exp_f32_e32 v105, v105
	v_exp_f32_e32 v106, v106
	v_exp_f32_e32 v107, v107
	v_exp_f32_e32 v108, v108
	v_exp_f32_e32 v109, v109
	v_exp_f32_e32 v110, v110
	v_exp_f32_e32 v111, v111
	v_exp_f32_e32 v112, v112
	v_exp_f32_e32 v113, v113
	ds_read_b128 v[192:195], v219
	ds_read_b128 v[196:199], v219 offset:16
	v_pk_add_f32 v[66:67], v[232:233], v[98:99]
	v_pk_add_f32 v[68:69], v[230:231], v[100:101]
	v_pk_add_f32 v[66:67], v[102:103], v[66:67]
	v_pk_add_f32 v[68:69], v[104:105], v[68:69]
	v_pk_add_f32 v[66:67], v[106:107], v[66:67]
	v_pk_add_f32 v[68:69], v[108:109], v[68:69]
	v_pk_add_f32 v[140:141], v[110:111], v[66:67]
	v_pk_add_f32 v[138:139], v[112:113], v[68:69]
	v_mfma_f32_32x32x64_f8f6f4 v[18:33], v[146:153], v[130:137], v[18:33]
	v_exp_f32_e32 v82, v82
	v_exp_f32_e32 v83, v83
	v_exp_f32_e32 v84, v84
	v_exp_f32_e32 v85, v85
	v_exp_f32_e32 v86, v86
	v_exp_f32_e32 v87, v87
	v_exp_f32_e32 v88, v88
	v_exp_f32_e32 v89, v89
	v_exp_f32_e32 v90, v90
	v_exp_f32_e32 v91, v91
	v_exp_f32_e32 v92, v92
	v_exp_f32_e32 v93, v93
	v_exp_f32_e32 v94, v94
	v_exp_f32_e32 v95, v95
	v_exp_f32_e32 v96, v96
	v_exp_f32_e32 v97, v97
	v_pk_add_f32 v[66:67], v[190:191], v[82:83]
	v_pk_add_f32 v[68:69], v[188:189], v[84:85]
	v_pk_add_f32 v[66:67], v[86:87], v[66:67]
	v_pk_add_f32 v[68:69], v[88:89], v[68:69]
	v_pk_add_f32 v[130:131], v[90:91], v[66:67]
	v_pk_add_f32 v[132:133], v[92:93], v[68:69]
	s_waitcnt lgkmcnt(0)
; DI void attn_unit_a8(unsigned char* lds, const AttnArgs& a) {
;     ...
;     auto w_decode = [&](int j, const float*& src, unsigned char*& dst, int& ld, int& n0, int& k0, bool& gu) __attribute__((always_inline)) {
;         const int g = (j >> 2) * 512 + a.wl, e = g / 96, rr = g - e * 96; KParamsPtr kp = kparams();
;         if (rr < 64) { src = kp->w_gu + ((size_t)a.wli * NE + e) * (1024 * 2048); dst = kp->ws + WS_WGU + (size_t)a.wli * SZ_WGU + (size_t)e * 2048 * 1024; ld = 2048; n0 = (rr & 7) * 256; k0 = ((rr >> 3) * 4 + (j & 3)) * 32; gu = true; }
;         else { const int q = rr - 64; src = kp->w_dn + ((size_t)a.wli * NE + e) * (1024 * 1024); dst = kp->ws + WS_WDN + (size_t)a.wli * SZ_WDN + (size_t)e * 1024 * 1024; ld = 1024; n0 = (q & 3) * 256; k0 = ((q >> 2) * 4 + (j & 3)) * 32; gu = false; } };
;     auto w_issue = [&](int j) __attribute__((always_inline)) { const float* src; unsigned char* dst; int ld, n0, k0; bool gu; w_decode(j, src, dst, ld, n0, k0, gu);
;         const float* p = src + (size_t)(k0 + 4 * wid) * ld + n0 + wn4;
;         wq[0] = __builtin_nontemporal_load((const f32x4*)p); wq[1] = __builtin_nontemporal_load((const f32x4*)(p + ld));
;         wq[2] = __builtin_nontemporal_load((const f32x4*)(p + (size_t)2 * ld)); wq[3] = __builtin_nontemporal_load((const f32x4*)(p + (size_t)3 * ld)); };
;     auto w_cvt = [&]() __attribute__((always_inline)) { unsigned char* t8 = lds + AT_WT + wn4 * WPITCH + 4 * wid;
; #pragma unroll
; DI void attn_unit_d8(unsigned char* lds, const AttnArgs& a) {
;     ...
;     auto tile = [&](const unsigned char* Kb, const unsigned char* Kn, v8i& Pa, v8i& Pb, v8i& v0, v8i& v1, const v8i& Qa, const v8i& Qb, const v8i& w0, const v8i& w1) __attribute__((always_inline)) {
;         qk(Kb, 1, s1a, s1b);
;         v0 = rd32(Kb + voff); v1 = rd32(Kb + voff + 32 * A8_PITCH);
;         o0[0] = mfma8(w0, Qa, o0[0]); o1[0] = mfma8(w0, Qb, o1[0]); o0[1] = mfma8(w1, Qa, o0[1]); o1[1] = mfma8(w1, Qb, o1[1]);
;         expsum(s0a, l0); expsum(s0b, l1); pack4(s0a, Pa, 0); pack4(s0b, Pb, 0);
;         qk(Kn, 0, s0a, s0b);
;         expsum(s1a, l0); expsum(s1b, l1); pack4(s1a, Pa, 4); pack4(s1b, Pb, 4);
; #pragma unroll
;         for (int i = 0; i < 8; ++i) { __builtin_amdgcn_sched_group_barrier(0x008, 1, 0); __builtin_amdgcn_sched_group_barrier(0x402, 22, 0); }
;     };
	v_mfma_f32_32x32x64_f8f6f4 v[66:81], v[192:199], v[114:121], 0
	s_nop 0
	s_nop 0
	s_nop 0
	s_nop 0
	s_nop 0
	s_nop 0
	s_nop 0
	v_cvt_scalef32_pk_fp8_f32 v188, v98, v99, s36
	v_cvt_scalef32_pk_fp8_f32 v189, v102, v103, s36
	v_cvt_scalef32_pk_fp8_f32 v190, v106, v107, s36
	v_cvt_scalef32_pk_fp8_f32 v191, v110, v111, s36
	v_cvt_scalef32_pk_fp8_f32 v158, v82, v83, s36
	v_cvt_scalef32_pk_fp8_f32 v159, v86, v87, s36
	v_pk_add_f32 v[142:143], v[96:97], v[132:133]
	v_pk_add_f32 v[144:145], v[94:95], v[130:131]
	v_cvt_scalef32_pk_fp8_f32 v160, v90, v91, s36
	v_cvt_scalef32_pk_fp8_f32 v188, v100, v101, s36 op_sel:[0,0,0,1]
	v_cvt_scalef32_pk_fp8_f32 v189, v104, v105, s36 op_sel:[0,0,0,1]
	v_cvt_scalef32_pk_fp8_f32 v190, v108, v109, s36 op_sel:[0,0,0,1]
	v_cvt_scalef32_pk_fp8_f32 v191, v112, v113, s36 op_sel:[0,0,0,1]
	v_cvt_scalef32_pk_fp8_f32 v158, v84, v85, s36 op_sel:[0,0,0,1]
	v_cvt_scalef32_pk_fp8_f32 v159, v88, v89, s36 op_sel:[0,0,0,1]
	v_mfma_f32_32x32x64_f8f6f4 v[98:113], v[192:199], v[122:129], 0
	global_load_dwordx2 v[192:193], v[220:221], off
	global_load_dwordx2 v[194:195], v[222:223], off
	ds_read_b128 v[130:133], v219 offset:2560
	ds_read_b128 v[134:137], v219 offset:2576
	s_mulk_i32 s19, 0x2800
	s_nop 0
	v_exp_f32_e32 v146, v66
	s_lshr_b32 s73, s61, 2
	v_exp_f32_e32 v147, v67
	s_add_i32 s73, s73, 3
	v_exp_f32_e32 v148, v68
	s_lshl_b32 s73, s73, 9
	v_exp_f32_e32 v149, v69
	s_add_i32 s73, s73, s42
	s_add_i32 s19, s19, 0
	v_cvt_scalef32_pk_fp8_f32 v161, v94, v95, s36
	v_exp_f32_e32 v150, v70
	s_mul_i32 s75, s73, 0xaaab
	v_exp_f32_e32 v151, v71
	s_lshr_b32 s75, s75, 22
	v_exp_f32_e32 v152, v72
	s_mul_i32 s76, s75, 0x60
	v_exp_f32_e32 v153, v73
	s_sub_i32 s76, s73, s76
	v_add_u32_e32 v224, s19, v216
	v_add_u32_e32 v225, s19, v217
	v_cvt_scalef32_pk_fp8_f32 v160, v92, v93, s36 op_sel:[0,0,0,1]
	v_cvt_scalef32_pk_fp8_f32 v161, v96, v97, s36 op_sel:[0,0,0,1]
	v_exp_f32_e32 v196, v74
	s_lshr_b32 s77, s76, 6
	v_exp_f32_e32 v197, v75
	s_lshl_b32 s78, s77, 6
	v_exp_f32_e32 v198, v76
	s_sub_i32 s76, s76, s78
	v_exp_f32_e32 v199, v77
	s_sub_i32 s78, 3, s77
	v_exp_f32_e32 v200, v78
	s_lshr_b32 s79, s76, s78
	v_exp_f32_e32 v201, v79
	s_lshl_b32 s79, s79, 2
	v_exp_f32_e32 v220, v80
	s_and_b32 s81, s61, 3
	v_exp_f32_e32 v221, v81
	s_add_i32 s79, s79, s81
	s_waitcnt lgkmcnt(0)
	v_mfma_f32_32x32x64_f8f6f4 v[82:97], v[130:137], v[114:121], 0
	v_add_f32_e64 v66, v140, v146
	v_add_f32_e64 v67, v141, v147
	v_add_f32_e64 v68, v138, v148
	v_add_f32_e64 v69, v139, v149
	v_add_f32_e64 v66, v150, v66
	v_add_f32_e64 v67, v151, v67
	v_add_f32_e64 v68, v152, v68
	v_add_f32_e64 v69, v153, v69
	v_add_f32_e64 v138, v196, v66
	v_add_f32_e64 v139, v197, v67
	v_add_f32_e64 v140, v198, v68
	v_add_f32_e64 v141, v199, v69
	v_exp_f32_e32 v98, v98
	s_lshl_b32 s79, s79, 5
	v_exp_f32_e32 v99, v99
	s_lshl_b32 s81, s63, 2
	v_exp_f32_e32 v100, v100
	s_add_i32 s81, s81, s79
	v_exp_f32_e32 v101, v101
	s_sub_i32 s78, 13, s77
	v_exp_f32_e32 v102, v102
	s_lshl_b32 s81, s81, s78
	v_exp_f32_e32 v103, v103
	s_lshr_b32 s78, 7, s77
	v_exp_f32_e32 v104, v104
	s_and_b32 s78, s76, s78
	v_exp_f32_e32 v105, v105
	s_lshl_b32 s72, s78, 10
	v_exp_f32_e32 v106, v106
	s_add_i32 s81, s81, s72
	v_exp_f32_e32 v107, v107
	s_add_i32 s72, s75, 0
	v_exp_f32_e32 v108, v108
	s_sub_i32 s80, 23, s77
	v_exp_f32_e32 v109, v109
	s_lshl_b32 s72, s72, s80
	v_exp_f32_e32 v110, v110
	s_add_i32 s81, s81, s72
	v_exp_f32_e32 v111, v111
	s_cmp_eq_u32 s77, 0
	s_cselect_b64 s[84:85], s[66:67], s[68:69]
	v_exp_f32_e32 v112, v112
	s_add_u32 s84, s84, s81
	s_addc_u32 s85, s85, 0
	v_exp_f32_e32 v113, v113
	s_lshr_b32 s80, 0x2000, s77
	v_mfma_f32_32x32x64_f8f6f4 v[66:81], v[130:137], v[122:129], 0
	v_add_f32_e64 v130, v144, v98
	v_add_f32_e64 v131, v145, v99
	v_add_f32_e64 v132, v142, v100
	v_add_f32_e64 v133, v143, v101
	v_add_f32_e64 v142, v102, v130
	v_add_f32_e64 v143, v103, v131
	v_add_f32_e64 v132, v104, v132
	v_add_f32_e64 v133, v105, v133
	v_add_f32_e64 v134, v220, v140
	v_add_f32_e64 v135, v221, v141
	v_add_f32_e64 v136, v200, v138
	v_add_f32_e64 v137, v201, v139
	s_nop 0
	s_nop 0
	s_nop 0
	s_nop 0
	s_nop 0
	s_nop 0
	v_pk_add_f32 v[142:143], v[106:107], v[142:143]
	v_pk_add_f32 v[132:133], v[108:109], v[132:133]
	v_cvt_scalef32_pk_fp8_f32 v138, v146, v147, s36
	v_cvt_scalef32_pk_fp8_f32 v139, v150, v151, s36
	v_cvt_scalef32_pk_fp8_f32 v140, v196, v197, s36
	v_cvt_scalef32_pk_fp8_f32 v141, v200, v201, s36
	v_cvt_scalef32_pk_fp8_f32 v130, v98, v99, s36
	v_cvt_scalef32_pk_fp8_f32 v131, v102, v103, s36
	v_pk_add_f32 v[146:147], v[112:113], v[132:133]
	v_pk_add_f32 v[150:151], v[110:111], v[142:143]
	v_mfma_f32_32x32x64_f8f6f4 v[50:65], v[170:177], v[184:191], v[50:65]
	v_exp_f32_e32 v82, v82
	s_and_b32 s72, s78, 3
	v_exp_f32_e32 v83, v83
	s_lshl_b32 s72, s72, 19
	v_exp_f32_e32 v84, v84
	s_lshr_b32 s81, s78, 2
	v_exp_f32_e32 v85, v85
	s_lshl_b32 s81, s81, 17
	v_add_u32_e32 v102, s17, v218
	v_exp_f32_e32 v86, v86
	s_add_i32 s72, s72, s81
	v_exp_f32_e32 v87, v87
	s_lshl_b32 s81, s78, 18
	v_exp_f32_e32 v88, v88
	s_cmp_eq_u32 s77, 0
	s_cselect_b32 s72, s72, s81
; DI unsigned pk4_fp8_mul64(float a, float b, float c, float d) { v2s_t r = {0, 0}; r = __builtin_amdgcn_cvt_scalef32_pk_fp8_f32(r, a, b, 0.015625f, false); r = __builtin_amdgcn_cvt_scalef32_pk_fp8_f32(r, c, d, 0.015625f, true); return __builtin_bit_cast(unsigned, r); }
; DI f32x16 mfma8(v8i a, v8i b, f32x16 c) { return __builtin_amdgcn_mfma_scale_f32_32x32x64_f8f6f4(a, b, c, 0, 0, 0, 0, 0, 0); }
; DI void attn_unit_a8(unsigned char* lds, const AttnArgs& a) {
;     ...
;     auto w_cvt = [&]() __attribute__((always_inline)) { unsigned char* t8 = lds + AT_WT + wn4 * WPITCH + 4 * wid;
; #pragma unroll
;         for (int j = 0; j < 4; ++j) *(unsigned*)(t8 + j * WPITCH) = pk4_fp8_mul64(wq[0][j], wq[1][j], wq[2][j], wq[3][j]); };
;     const int wcol = tid >> 1, whalf = tid & 1;
;     const unsigned wper_gu = (unsigned)((wcol >> 7) * 256 + (wcol & 96) + invperm32(wcol & 31)) * 1024u + 16u * whalf;
;     const unsigned wper_dn = (unsigned)fwd_lane16(wcol) * 1024u + 16u * whalf;
;     auto w_store = [&](int j) __attribute__((always_inline)) { const float* src; unsigned char* dst; int ld, n0, k0; bool gu; w_decode(j, src, dst, ld, n0, k0, gu);
;         const int nb = n0 >> 8; const unsigned uni = (unsigned)(gu ? (nb & 3) * 512 + (nb >> 2) * 128 : nb * 256) * 1024u + (unsigned)k0;
;         const unsigned off = (gu ? wper_gu : wper_dn) + uni;
;         const unsigned* t = (const unsigned*)(lds + AT_WT + wcol * WPITCH + 16 * whalf);
;         *(u32x4*)(dst + off) = (u32x4){t[0], t[1], t[2], t[3]}; };
; DI void attn_unit_d8(unsigned char* lds, const AttnArgs& a) {
;     ...
;     auto tile = [&](const unsigned char* Kb, const unsigned char* Kn, v8i& Pa, v8i& Pb, v8i& v0, v8i& v1, const v8i& Qa, const v8i& Qb, const v8i& w0, const v8i& w1) __attribute__((always_inline)) {
;         qk(Kb, 1, s1a, s1b);
;         v0 = rd32(Kb + voff); v1 = rd32(Kb + voff + 32 * A8_PITCH);
;         o0[0] = mfma8(w0, Qa, o0[0]); o1[0] = mfma8(w0, Qb, o1[0]); o0[1] = mfma8(w1, Qa, o0[1]); o1[1] = mfma8(w1, Qb, o1[1]);
;         expsum(s0a, l0); expsum(s0b, l1); pack4(s0a, Pa, 0); pack4(s0b, Pb, 0);
;         qk(Kn, 0, s0a, s0b);
;         expsum(s1a, l0); expsum(s1b, l1); pack4(s1a, Pa, 4); pack4(s1b, Pb, 4);
; #pragma unroll
;         for (int i = 0; i < 8; ++i) { __builtin_amdgcn_sched_group_barrier(0x008, 1, 0); __builtin_amdgcn_sched_group_barrier(0x402, 22, 0); }
;     };
	v_exp_f32_e32 v89, v89
	s_mul_i32 s81, s77, 0x10000000
	v_cvt_scalef32_pk_fp8_f32 v130, v100, v101, s36 op_sel:[0,0,0,1]
	v_cvt_scalef32_pk_fp8_f32 v131, v104, v105, s36 op_sel:[0,0,0,1]
	v_exp_f32_e32 v90, v90
	s_add_i32 s81, s81, 0x1094000
	v_exp_f32_e32 v91, v91
	s_add_i32 s72, s72, s79
	v_exp_f32_e32 v92, v92
	s_sub_i32 s73, 21, s77
	v_exp_f32_e32 v93, v93
	s_lshl_b32 s73, s75, s73
	ds_read_b128 v[98:101], v102
	ds_read_b128 v[102:105], v102 offset:16
	s_nop 0
	v_cvt_scalef32_pk_fp8_f32 v138, v148, v149, s36 op_sel:[0,0,0,1]
	v_cvt_scalef32_pk_fp8_f32 v139, v152, v153, s36 op_sel:[0,0,0,1]
	v_cvt_scalef32_pk_fp8_f32 v140, v198, v199, s36 op_sel:[0,0,0,1]
	v_cvt_scalef32_pk_fp8_f32 v141, v220, v221, s36 op_sel:[0,0,0,1]
	s_nop 0
	v_exp_f32_e32 v94, v94
	s_add_i32 s72, s72, s73
	v_mfma_f32_32x32x64_f8f6f4 v[2:17], v[170:177], v[154:161], v[2:17]
	v_exp_f32_e32 v148, v96
	s_add_u32 s72, s72, s81
	v_cvt_scalef32_pk_fp8_f32 v132, v106, v107, s36
	v_exp_f32_e32 v149, v97
	s_or_b32 s79, s72, s77
	v_pk_add_f32 v[96:97], v[136:137], v[82:83]
	v_pk_add_f32 v[106:107], v[134:135], v[84:85]
	v_exp_f32_e32 v66, v66
	v_exp_f32_e32 v67, v67
	v_exp_f32_e32 v68, v68
	v_exp_f32_e32 v69, v69
	v_exp_f32_e32 v95, v95
	v_cvt_scalef32_pk_fp8_f32 v133, v110, v111, s36
	v_pk_add_f32 v[106:107], v[88:89], v[106:107]
	v_pk_add_f32 v[96:97], v[86:87], v[96:97]
	v_exp_f32_e32 v70, v70
	v_exp_f32_e32 v71, v71
	v_exp_f32_e32 v72, v72
	v_exp_f32_e32 v73, v73
	v_cvt_scalef32_pk_fp8_f32 v132, v108, v109, s36 op_sel:[0,0,0,1]
	v_cvt_scalef32_pk_fp8_f32 v133, v112, v113, s36 op_sel:[0,0,0,1]
	v_pk_add_f32 v[96:97], v[90:91], v[96:97]
	v_pk_add_f32 v[106:107], v[92:93], v[106:107]
	v_exp_f32_e32 v74, v74
	v_mfma_f32_32x32x64_f8f6f4 v[34:49], v[162:169], v[184:191], v[34:49]
	v_exp_f32_e32 v75, v75
	v_exp_f32_e32 v76, v76
	v_exp_f32_e32 v77, v77
	v_exp_f32_e32 v78, v78
	v_exp_f32_e32 v79, v79
	s_nop 0
	v_exp_f32_e32 v80, v80
	v_exp_f32_e32 v81, v81
	s_nop 0
	s_nop 0
	v_cvt_scalef32_pk_fp8_f32 v142, v82, v83, s36
	s_nop 0
	v_cvt_scalef32_pk_fp8_f32 v143, v86, v87, s36
	v_cvt_scalef32_pk_fp8_f32 v144, v90, v91, s36
	v_cvt_scalef32_pk_fp8_f32 v142, v84, v85, s36 op_sel:[0,0,0,1]
	v_pk_add_f32 v[82:83], v[150:151], v[66:67]
	v_pk_add_f32 v[84:85], v[146:147], v[68:69]
	s_mulk_i32 s49, 0x2800
	v_pk_add_f32 v[184:185], v[148:149], v[106:107]
	v_pk_add_f32 v[186:187], v[94:95], v[96:97]
	v_cvt_scalef32_pk_fp8_f32 v145, v94, v95, s36
	v_cvt_scalef32_pk_fp8_f32 v143, v88, v89, s36 op_sel:[0,0,0,1]
	v_cvt_scalef32_pk_fp8_f32 v144, v92, v93, s36 op_sel:[0,0,0,1]
	v_mfma_f32_32x32x64_f8f6f4 v[18:33], v[162:169], v[154:161], v[18:33]
	v_add_f32_e64 v84, v72, v84
	v_add_f32_e64 v85, v73, v85
	v_add_f32_e64 v82, v70, v82
	v_add_f32_e64 v83, v71, v83
	s_nop 0
	s_nop 0
	s_nop 0
	s_nop 0
	s_add_i32 s6, s49, 0
	v_add_f32_e64 v82, v74, v82
	v_add_f32_e64 v83, v75, v83
	v_add_f32_e64 v84, v76, v84
	v_add_f32_e64 v85, v77, v85
	v_cvt_scalef32_pk_fp8_f32 v134, v66, v67, s36
	v_cvt_scalef32_pk_fp8_f32 v135, v70, v71, s36
	v_cvt_scalef32_pk_fp8_f32 v136, v74, v75, s36
	v_cvt_scalef32_pk_fp8_f32 v137, v78, v79, s36
	v_pk_add_f32 v[188:189], v[80:81], v[84:85]
	v_pk_add_f32 v[190:191], v[78:79], v[82:83]
	v_add_u32_e32 v106, s6, v216
	v_add_u32_e32 v107, s6, v217
	v_cvt_scalef32_pk_fp8_f32 v145, v148, v149, s36 op_sel:[0,0,0,1]
	v_cvt_scalef32_pk_fp8_f32 v134, v68, v69, s36 op_sel:[0,0,0,1]
	v_cvt_scalef32_pk_fp8_f32 v135, v72, v73, s36 op_sel:[0,0,0,1]
	v_cvt_scalef32_pk_fp8_f32 v136, v76, v77, s36 op_sel:[0,0,0,1]
	v_cvt_scalef32_pk_fp8_f32 v137, v80, v81, s36 op_sel:[0,0,0,1]
	s_waitcnt lgkmcnt(0)
	v_mfma_f32_32x32x64_f8f6f4 v[82:97], v[98:105], v[114:121], 0
	ds_read_b128 v[154:157], v219 offset:5120
	ds_read_b128 v[158:161], v219 offset:5136
	ds_read_b128 v[146:149], v219 offset:7680
	ds_read_b128 v[150:153], v219 offset:7696
	s_cmpk_gt_i32 s42, 0x1ff
	s_cbranch_scc1 .Lmy_rd0_ldum
	s_add_i32 s72, s61, -1
	s_cmp_lt_u32 s72, 12
	s_cbranch_scc0 .Lmy_rd0_noc
	s_waitcnt vmcnt(4)
	v_cvt_scalef32_pk_fp8_f32 v236, v236, v240, s62
	v_cvt_scalef32_pk_fp8_f32 v237, v237, v241, s62
	v_cvt_scalef32_pk_fp8_f32 v238, v238, v242, s62
	v_cvt_scalef32_pk_fp8_f32 v239, v239, v243, s62
	v_cvt_scalef32_pk_fp8_f32 v236, v244, v248, s62 op_sel:[0,0,0,1]
	v_cvt_scalef32_pk_fp8_f32 v237, v245, v249, s62 op_sel:[0,0,0,1]
	v_cvt_scalef32_pk_fp8_f32 v238, v246, v250, s62 op_sel:[0,0,0,1]
	v_cvt_scalef32_pk_fp8_f32 v239, v247, v251, s62 op_sel:[0,0,0,1]
	ds_write_b32 v252, v236
	ds_write_b32 v252, v237 offset:36
	ds_write_b32 v252, v238 offset:72
	ds_write_b32 v252, v239 offset:108
.Lmy_rd0_noc:
	ds_read2_b32 v[244:245], v253 offset1:1
	ds_read2_b32 v[246:247], v253 offset0:2 offset1:3
	s_cmpk_gt_i32 s42, 0x1ff
	s_cbranch_scc1 .Lmy_rd0_sdum
	s_add_i32 s72, s61, -2
	s_cmp_lt_u32 s72, 12
	s_cbranch_scc0 .Lmy_rd0_sdum
	s_andn2_b32 s73, s65, 1
	s_add_u32 s82, s70, s73
	s_addc_u32 s83, s71, 0
	s_bitcmp1_b32 s65, 0
	s_cbranch_scc1 .Lmy_rd0_sdn
	s_waitcnt lgkmcnt(0)
	global_store_dwordx4 v254, v[244:247], s[82:83]
	s_branch .Lmy_rd0_sdone

; DI void attn_unit_a8(unsigned char* lds, const AttnArgs& a) {
;     ...
;     auto w_issue = [&](int j) __attribute__((always_inline)) { const float* src; unsigned char* dst; int ld, n0, k0; bool gu; w_decode(j, src, dst, ld, n0, k0, gu);
;         const float* p = src + (size_t)(k0 + 4 * wid) * ld + n0 + wn4;
;         wq[0] = __builtin_nontemporal_load((const f32x4*)p); wq[1] = __builtin_nontemporal_load((const f32x4*)(p + ld));
;         wq[2] = __builtin_nontemporal_load((const f32x4*)(p + (size_t)2 * ld)); wq[3] = __builtin_nontemporal_load((const f32x4*)(p + (size_t)3 * ld)); };
.Lmy_rd0_sdone:
	s_cmpk_gt_i32 s42, 0x1ff
	s_cbranch_scc1 .Lmy_rd0_ld0
	s_cmp_lt_u32 s61, 12
	s_cbranch_scc1 .Lmy_rd0_lgo

; DI void attn_unit_a8(unsigned char* lds, const AttnArgs& a) {
;     ...
;     auto w_issue = [&](int j) __attribute__((always_inline)) { const float* src; unsigned char* dst; int ld, n0, k0; bool gu; w_decode(j, src, dst, ld, n0, k0, gu);
;         const float* p = src + (size_t)(k0 + 4 * wid) * ld + n0 + wn4;
;         wq[0] = __builtin_nontemporal_load((const f32x4*)p); wq[1] = __builtin_nontemporal_load((const f32x4*)(p + ld));
;         wq[2] = __builtin_nontemporal_load((const f32x4*)(p + (size_t)2 * ld)); wq[3] = __builtin_nontemporal_load((const f32x4*)(p + (size_t)3 * ld)); };
;     auto w_cvt = [&]() __attribute__((always_inline)) { unsigned char* t8 = lds + AT_WT + wn4 * WPITCH + 4 * wid;
; #pragma unroll
;         for (int j = 0; j < 4; ++j) *(unsigned*)(t8 + j * WPITCH) = pk4_fp8_mul64(wq[0][j], wq[1][j], wq[2][j], wq[3][j]); };
;     const int wcol = tid >> 1, whalf = tid & 1;
;     const unsigned wper_gu = (unsigned)((wcol >> 7) * 256 + (wcol & 96) + invperm32(wcol & 31)) * 1024u + 16u * whalf;
;     const unsigned wper_dn = (unsigned)fwd_lane16(wcol) * 1024u + 16u * whalf;
;     ...
;     auto step = [&](int t, u32x2& kl, u32x2& vl, const u32x2& ks, const u32x2& vs, f32x16& c0, f32x16& c1, f32x16& n0, f32x16& n1, const int hk, const int wj) __attribute__((always_inline)) {
;         const int slot1 = slot == 2 ? 0 : slot + 1, slot2 = slot1 == 2 ? 0 : slot1 + 1;
;         if (hk == 1) { w_cvt(); w_issue(wj + 1 < AT_NWT ? wj + 1 : AT_NWT - 1); }
;         if (hk == 2) w_store(wj);
;         { const int tn = t + 3; gload(tn < a.t1 ? tn : a.t1 - 1, kl, vl); }
;         const unsigned char* Kb = lds + slot * AT_BUFB; const unsigned char* Kn = lds + slot1 * AT_BUFB;
;         const v8i k0 = kread(Kn, 0), k1 = kread(Kn, 1), v0 = vread(Kb, 0), v1 = vread(Kb, 1);
;         n0 = mfma8(k0, qf8, cinit); n1 = mfma8(k1, qf8, cinit);
;         expsum(c0); expsum(c1);
;         const v8i P = pack8(c0, c1);
;         o0[0] = mfma8(v0, P, o0[0]); o0[1] = mfma8(v1, P, o0[1]);
;         lstore(slot2, ks, vs);
;         __syncthreads();
;         slot = slot1;
;     };
;     {
;         int t = a.t0;
;         if (wrider)
;             for (int j = 0; j < AT_NWT; ++j, t += 2) { step(t, kregB, vregB, kregA, vregA, sx0, sx1, sy0, sy1, 1, j); step(t + 1, kregA, vregA, kregB, vregB, sy0, sy1, sx0, sx1, 2, j); }
.LBB0_702:
	s_lshl_b32 s4, s14, 1
	s_waitcnt lgkmcnt(0)
	s_lshr_b32 s12, s14, 3
	s_and_b32 s4, s4, 0x600
	s_and_b32 s12, s12, 0x80
	s_or_b32 s4, s4, s12
	s_and_b64 s[10:11], s[10:11], exec
	s_cselect_b32 s4, s4, s14
	s_and_b32 s10, s24, 3
	s_add_i32 s10, s63, s10
	s_lshl_b32 s10, s10, 5
	s_lshl_b32 s4, s4, 10
	s_add_i32 s15, s4, s10
	s_min_i32 s4, s56, 63
	s_cmp_lt_u32 s56, 60
	s_cselect_b64 s[10:11], -1, 0
	s_lshl_b32 s4, s4, 6
	v_pk_add_f32 v[48:49], v[146:147], v[110:111]
	s_add_i32 s14, s4, 0x100
	s_add_i32 s63, s4, 0xfffff100
	v_pk_add_f32 v[46:47], v[150:151], v[108:109]
	v_pk_add_f32 v[48:49], v[148:149], v[48:49]
	s_and_b64 s[12:13], s[10:11], exec
	v_pk_add_f32 v[46:47], v[142:143], v[46:47]
	v_pk_add_f32 v[48:49], v[58:59], v[48:49]
	s_cselect_b32 s12, s14, s63
	s_add_i32 s25, s25, 1
	v_pk_add_f32 v[46:47], v[144:145], v[46:47]
	v_pk_add_f32 v[48:49], v[60:61], v[48:49]
	s_and_b64 s[6:7], s[6:7], exec
	v_pk_add_f32 v[46:47], v[52:53], v[46:47]
	v_pk_add_f32 v[48:49], v[50:51], v[48:49]
	s_cselect_b32 s14, 0, s25
	v_pk_add_f32 v[46:47], v[56:57], v[46:47]
	v_pk_add_f32 v[48:49], v[54:55], v[48:49]
	s_mul_i32 s6, s14, 0x4680
	v_pk_add_f32 v[38:39], v[38:39], v[46:47]
	v_pk_add_f32 v[36:37], v[36:37], v[48:49]
	v_add_u32_e32 v48, 0xd808, v163
	v_add_u32_e32 v134, s6, v157
	v_pk_add_f32 v[50:51], v[42:43], v[38:39]
	v_pk_add_f32 v[108:109], v[40:41], v[36:37]
	v_add_u32_e32 v45, 0xd800, v163
	ds_read_b128 v[36:39], v134
	ds_read_b128 v[40:43], v134 offset:16
	ds_read2_b32 v[46:47], v45 offset1:1
	ds_read2_b32 v[48:49], v48 offset1:1
	v_pk_add_f32 v[110:111], v[34:35], v[50:51]
	v_add_u32_e32 v34, v44, v158
	v_lshl_or_b32 v34, v34, 10, v160
	v_add_u32_e32 v34, s15, v34
	s_waitcnt lgkmcnt(0)
	global_store_dwordx4 v34, v[46:49], s[8:9]
	v_add_u32_e32 v34, s12, v154
	s_and_b64 s[8:9], s[10:11], exec
	v_ashrrev_i32_e32 v35, 31, v34
	s_cselect_b32 s9, s59, s61
	s_cselect_b32 s8, s58, s60
	v_lshlrev_b64 v[34:35], 7, v[34:35]
	v_mfma_f32_32x32x64_f8f6f4 v[50:65], v[36:43], v[98:105], 0
	v_lshl_add_u64 v[42:43], s[8:9], 0, v[34:35]
	v_lshl_add_u64 v[42:43], v[42:43], 0, v[130:131]
	ds_read_b128 v[34:37], v134 offset:2560
	ds_read_b128 v[38:41], v134 offset:2576
	global_load_dwordx2 v[134:135], v[42:43], off
	v_lshl_add_u64 v[42:43], v[132:133], 0, s[4:5]
	global_load_dwordx2 v[136:137], v[42:43], off offset:256
	v_exp_f32_e32 v82, v82
	v_exp_f32_e32 v83, v83
	v_exp_f32_e32 v86, v86
	v_exp_f32_e32 v87, v87
	v_exp_f32_e32 v90, v90
	v_exp_f32_e32 v91, v91
	v_exp_f32_e32 v94, v94
	v_exp_f32_e32 v95, v95
	v_exp_f32_e32 v150, v66
	v_exp_f32_e32 v151, v67
	v_exp_f32_e32 v174, v70
	v_exp_f32_e32 v175, v71
	v_exp_f32_e32 v74, v74
	v_exp_f32_e32 v75, v75
	v_exp_f32_e32 v78, v78
	v_exp_f32_e32 v79, v79
	ds_read_b128 v[142:145], v164 offset:5120
	ds_read_b128 v[146:149], v164 offset:5136
	ds_read_b128 v[166:169], v164 offset:7680
	ds_read_b128 v[170:173], v164 offset:7696
	v_exp_f32_e32 v84, v84
	v_exp_f32_e32 v85, v85
	v_exp_f32_e32 v88, v88
	v_exp_f32_e32 v89, v89
	v_exp_f32_e32 v92, v92
	v_exp_f32_e32 v93, v93
	v_exp_f32_e32 v96, v96
	v_exp_f32_e32 v97, v97
	v_exp_f32_e32 v164, v68
	v_exp_f32_e32 v165, v69
	v_exp_f32_e32 v176, v72
	v_exp_f32_e32 v177, v73
	v_exp_f32_e32 v76, v76
	v_exp_f32_e32 v77, v77
	v_exp_f32_e32 v80, v80
	v_exp_f32_e32 v81, v81
	s_nop 0
	s_nop 0
	s_nop 0
	s_nop 0
	s_nop 0
	s_nop 0
	s_nop 0
	s_nop 0
	v_cvt_scalef32_pk_fp8_f32 v66, v82, v83, s48
	v_cvt_scalef32_pk_fp8_f32 v70, v150, v151, s48
	v_cvt_scalef32_pk_fp8_f32 v67, v86, v87, s48
	v_cvt_scalef32_pk_fp8_f32 v71, v174, v175, s48
	v_cvt_scalef32_pk_fp8_f32 v68, v90, v91, s48
	v_cvt_scalef32_pk_fp8_f32 v72, v74, v75, s48
	v_cvt_scalef32_pk_fp8_f32 v69, v94, v95, s48
	v_cvt_scalef32_pk_fp8_f32 v73, v78, v79, s48
	v_cvt_scalef32_pk_fp8_f32 v66, v84, v85, s48 op_sel:[0,0,0,1]
	v_cvt_scalef32_pk_fp8_f32 v70, v164, v165, s48 op_sel:[0,0,0,1]
	v_cvt_scalef32_pk_fp8_f32 v67, v88, v89, s48 op_sel:[0,0,0,1]
	v_cvt_scalef32_pk_fp8_f32 v71, v176, v177, s48 op_sel:[0,0,0,1]
	v_cvt_scalef32_pk_fp8_f32 v68, v92, v93, s48 op_sel:[0,0,0,1]
	v_cvt_scalef32_pk_fp8_f32 v72, v76, v77, s48 op_sel:[0,0,0,1]
	v_cvt_scalef32_pk_fp8_f32 v69, v96, v97, s48 op_sel:[0,0,0,1]
	v_cvt_scalef32_pk_fp8_f32 v73, v80, v81, s48 op_sel:[0,0,0,1]
	s_waitcnt lgkmcnt(4)
	v_mfma_f32_32x32x64_f8f6f4 v[34:49], v[34:41], v[98:105], 0
	v_add_f32_e64 v110, v110, v82
	v_add_f32_e64 v111, v111, v83
	v_add_f32_e64 v82, v108, v84
	v_add_f32_e64 v83, v109, v85
	v_add_f32_e64 v84, v86, v110
	v_add_f32_e64 v85, v87, v111
	v_add_f32_e64 v82, v88, v82
	v_add_f32_e64 v83, v89, v83
	s_addk_i32 s6, 0x4680
	v_add_f32_e64 v84, v90, v84
	v_add_f32_e64 v85, v91, v85
	v_add_f32_e64 v82, v92, v82
	v_add_f32_e64 v83, v93, v83
	s_cmp_lg_u32 s14, 2
	v_pk_add_f32 v[82:83], v[96:97], v[82:83]
	v_pk_add_f32 v[84:85], v[94:95], v[84:85]
	s_cselect_b32 s4, s6, 0
	v_pk_add_f32 v[84:85], v[150:151], v[84:85]
	v_pk_add_f32 v[82:83], v[164:165], v[82:83]
	s_add_i32 s4, s4, 0
	v_pk_add_f32 v[82:83], v[176:177], v[82:83]
	s_waitcnt lgkmcnt(2)
	v_mfma_f32_32x32x64_f8f6f4 v[18:33], v[142:149], v[66:73], v[18:33]
	v_add_f32_e64 v84, v174, v84
	v_add_f32_e64 v85, v175, v85
	v_add_f32_e64 v76, v76, v82
	v_add_f32_e64 v77, v77, v83
	v_add_f32_e64 v74, v74, v84
	v_add_f32_e64 v75, v75, v85
	s_add_i32 s24, s24, 1
	s_add_i32 s56, s56, 2
	s_addk_i32 s19, 0x80
	v_add_f32_e64 v110, v80, v76
	v_add_f32_e64 v111, v81, v77
	v_add_f32_e64 v108, v78, v74
	v_add_f32_e64 v109, v79, v75
	s_cmp_lg_u32 s24, 12
	s_waitcnt lgkmcnt(0)
	v_mfma_f32_32x32x64_f8f6f4 v[2:17], v[166:173], v[66:73], v[2:17]
	v_add_u32_e32 v66, s4, v155
	s_waitcnt vmcnt(4)
	ds_write_b64 v66, v[138:139]
	v_add_u32_e32 v66, s4, v156
	v_add_u32_e32 v66, 0x1400, v66
	s_waitcnt vmcnt(3)
	ds_write2_b32 v66, v140, v141 offset1:8
	s_waitcnt lgkmcnt(0)
	s_barrier
	s_cbranch_scc0 .LBB0_712
.LBB0_703:
	s_min_u32 s15, s24, 10
	s_add_i32 s15, s15, 1
	s_lshl_b32 s4, s15, 7
	s_and_b32 s4, s4, 0x1e00
	s_nop 0
	s_nop 0
	s_add_i32 s6, s4, s62
	v_cvt_scalef32_pk_fp8_f32 v66, v116, v112, s47
	v_cvt_scalef32_pk_fp8_f32 v67, v117, v113, s47
	s_mul_hi_u32 s4, s6, 0xaaaaaaab
	v_cvt_scalef32_pk_fp8_f32 v66, v120, v124, s47 op_sel:[0,0,0,1]
	v_cvt_scalef32_pk_fp8_f32 v67, v121, v125, s47 op_sel:[0,0,0,1]
	v_add_u32_e32 v68, 0xd800, v162
	s_lshr_b32 s4, s4, 6
	ds_write2_b32 v68, v66, v67 offset1:9
	s_nop 0
	s_nop 0
	s_mul_i32 s63, s4, 0xffffffa0
	v_cvt_scalef32_pk_fp8_f32 v66, v118, v114, s47
	v_cvt_scalef32_pk_fp8_f32 v67, v119, v115, s47
	s_add_i32 s63, s63, s6
	v_cvt_scalef32_pk_fp8_f32 v66, v122, v126, s47 op_sel:[0,0,0,1]
	v_cvt_scalef32_pk_fp8_f32 v67, v123, v127, s47 op_sel:[0,0,0,1]
	s_mov_b64 s[10:11], s[0:1]
	s_cmp_gt_i32 s63, 63
	s_mov_b64 s[12:13], -1
	ds_write2_b32 v68, v66, v67 offset0:18 offset1:27
	s_cbranch_scc0 .LBB0_705
	s_load_dwordx2 s[6:7], s[10:11], 0xc0
	s_lshl_b64 s[8:9], s[4:5], 22
	s_mov_b64 s[12:13], 0
	s_waitcnt lgkmcnt(0)
	s_add_u32 s6, s6, s8
	s_addc_u32 s7, s7, s9
	s_and_b32 s8, s63, 0x7ffffffc
	s_sub_i32 s25, s8, 64

; DI f32x16 mfma8(v8i a, v8i b, f32x16 c) { return __builtin_amdgcn_mfma_scale_f32_32x32x64_f8f6f4(a, b, c, 0, 0, 0, 0, 0, 0); }
; DI void attn_unit_d8(unsigned char* lds, const AttnArgs& a) {
;     ...
;     auto tile = [&](const unsigned char* Kb, const unsigned char* Kn, v8i& Pa, v8i& Pb, v8i& v0, v8i& v1, const v8i& Qa, const v8i& Qb, const v8i& w0, const v8i& w1) __attribute__((always_inline)) {
;         qk(Kb, 1, s1a, s1b);
;         v0 = rd32(Kb + voff); v1 = rd32(Kb + voff + 32 * A8_PITCH);
;         o0[0] = mfma8(w0, Qa, o0[0]); o1[0] = mfma8(w0, Qb, o1[0]); o0[1] = mfma8(w1, Qa, o0[1]); o1[1] = mfma8(w1, Qb, o1[1]);
;         expsum(s0a, l0); expsum(s0b, l1); pack4(s0a, Pa, 0); pack4(s0b, Pb, 0);
;         qk(Kn, 0, s0a, s0b);
;         expsum(s1a, l0); expsum(s1b, l1); pack4(s1a, Pa, 4); pack4(s1b, Pb, 4);
; #pragma unroll
;         for (int i = 0; i < 8; ++i) { __builtin_amdgcn_sched_group_barrier(0x008, 1, 0); __builtin_amdgcn_sched_group_barrier(0x402, 22, 0); }
;     };
;     for (int t = a.t0; t < a.t1; t += 2) {
;         const int s1 = sb + 1 >= 5 ? sb - 4 : sb + 1, s2 = sb + 2 >= 5 ? sb - 3 : sb + 2, s3 = sb + 3 >= 5 ? sb - 2 : sb + 3, s4 = sb + 4 >= 5 ? sb - 1 : sb + 4;
;         { const int ta = t + 3, tb = t + 4; gload(ta < a.t1 ? ta : a.t1 - 1, kreg0, vreg0); gload(tb < a.t1 ? tb : a.t1 - 1, kreg1, vreg1); }
;         tile(lds + sb * D8_SLOT, lds + s1 * D8_SLOT, PaX, PbX, vX0, vX1, PaY, PbY, vY0, vY1);
;         tile(lds + s1 * D8_SLOT, lds + s2 * D8_SLOT, PaY, PbY, vY0, vY1, PaX, PbX, vX0, vX1);
;         lstore(s3, kreg0, vreg0); lstore(s4, kreg1, vreg1);
;         __syncthreads();
;         sb = s2;
;     }
.LBB0_1888:
	s_add_i32 s22, s22, 2
	s_mul_i32 s8, s23, 0x2800
	s_cmp_gt_i32 s23, 3
	v_mfma_f32_32x32x64_f8f6f4 v[50:65], v[154:161], v[138:145], v[50:65]
	v_exp_f32_e32 v194, v90
	v_add_u32_e32 v90, s8, v219
	s_cselect_b32 s8, -4, 1
	s_add_i32 s51, s8, s23
	s_cmp_gt_i32 s23, 2
	s_cselect_b32 s8, -3, 2
	s_add_i32 s8, s8, s23
	s_cmp_gt_i32 s23, 1
	s_cselect_b32 s52, -2, 3
	s_add_i32 s52, s52, s23
	s_cmp_gt_i32 s23, 0
	s_cselect_b32 s53, -1, 4
	s_min_u32 s56, s22, 64
	s_add_i32 s53, s53, s23
	s_cmp_lt_u32 s22, 61
	s_mul_i32 s50, s8, 0x2800
	s_mov_b32 s23, s8
	s_cselect_b64 s[54:55], -1, 0
	s_lshl_b32 s8, s56, 6
	s_add_i32 s56, s8, 0xc0
	s_add_i32 s57, s8, 0xfffff0c0
	s_and_b64 s[54:55], s[54:55], exec
	v_lshl_add_u64 v[98:99], v[184:185], 0, s[8:9]
	s_cselect_b32 s8, s56, s57
	s_cselect_b32 s55, s19, s21
	s_cselect_b32 s54, s18, s20
	s_min_u32 s58, s22, 63
	v_exp_f32_e32 v200, v82
	v_exp_f32_e32 v201, v83
	v_exp_f32_e32 v198, v84
	v_exp_f32_e32 v199, v85
	v_exp_f32_e32 v202, v86
	v_exp_f32_e32 v203, v87
	v_exp_f32_e32 v196, v88
	v_exp_f32_e32 v197, v89
	ds_read_b128 v[82:85], v90 offset:2560
	ds_read_b128 v[86:89], v90 offset:2576
	global_load_dwordx2 v[204:205], v[98:99], off offset:192
	v_add_u32_e32 v98, s8, v182
	s_cmp_lt_u32 s22, 60
	v_ashrrev_i32_e32 v99, 31, v98
	s_cselect_b64 s[56:57], -1, 0
	s_lshl_b32 s8, s58, 6
	v_lshlrev_b64 v[98:99], 8, v[98:99]
	s_add_i32 s58, s8, 0x100
	s_add_i32 s59, s8, 0xfffff100
	v_lshl_add_u64 v[98:99], s[54:55], 0, v[98:99]
	s_and_b64 s[54:55], s[56:57], exec
	v_lshl_add_u64 v[100:101], v[184:185], 0, s[8:9]
	s_cselect_b32 s8, s58, s59
	v_lshl_add_u64 v[220:221], v[98:99], 0, v[178:179]
	v_add_u32_e32 v98, s8, v182
	v_ashrrev_i32_e32 v99, 31, v98
	s_cselect_b32 s55, s19, s21
	s_cselect_b32 s54, s18, s20
	v_lshlrev_b64 v[98:99], 8, v[98:99]
	v_lshl_add_u64 v[98:99], s[54:55], 0, v[98:99]
	global_load_dwordx2 v[206:207], v[100:101], off offset:256
	v_lshl_add_u64 v[222:223], v[98:99], 0, v[178:179]
	s_waitcnt lgkmcnt(0)
	v_mfma_f32_32x32x64_f8f6f4 v[98:113], v[82:89], v[114:121], 0
	v_exp_f32_e32 v195, v91
	v_exp_f32_e32 v224, v92
	v_exp_f32_e32 v225, v93
	v_exp_f32_e32 v226, v94
	v_exp_f32_e32 v227, v95
	v_exp_f32_e32 v228, v96
	v_exp_f32_e32 v229, v97
	ds_read_b128 v[170:173], v90 offset:5120
	ds_read_b128 v[174:177], v90 offset:5136
	ds_read_b128 v[162:165], v90 offset:7680
	ds_read_b128 v[166:169], v90 offset:7696
	v_pk_add_f32 v[90:91], v[188:189], v[200:201]
	v_pk_add_f32 v[92:93], v[186:187], v[198:199]
	v_pk_add_f32 v[90:91], v[202:203], v[90:91]
	v_pk_add_f32 v[92:93], v[196:197], v[92:93]
	v_pk_add_f32 v[90:91], v[194:195], v[90:91]
	v_pk_add_f32 v[92:93], v[224:225], v[92:93]
	v_exp_f32_e32 v66, v66
	v_exp_f32_e32 v67, v67
	v_exp_f32_e32 v68, v68
	v_exp_f32_e32 v69, v69
	v_exp_f32_e32 v70, v70
	v_exp_f32_e32 v71, v71
	v_exp_f32_e32 v72, v72
	v_pk_add_f32 v[230:231], v[228:229], v[92:93]
	v_pk_add_f32 v[232:233], v[226:227], v[90:91]
	v_mfma_f32_32x32x64_f8f6f4 v[82:97], v[82:89], v[122:129], 0
	v_exp_f32_e32 v73, v73
	v_exp_f32_e32 v74, v74
	v_exp_f32_e32 v75, v75
	v_exp_f32_e32 v76, v76
	v_exp_f32_e32 v77, v77
	v_exp_f32_e32 v78, v78
	v_exp_f32_e32 v79, v79
	v_exp_f32_e32 v80, v80
	v_exp_f32_e32 v81, v81
	v_pk_add_f32 v[188:189], v[192:193], v[66:67]
	v_pk_add_f32 v[190:191], v[190:191], v[68:69]
	s_nop 0
	v_pk_add_f32 v[188:189], v[70:71], v[188:189]
	v_pk_add_f32 v[190:191], v[72:73], v[190:191]
	s_nop 0
	v_cvt_scalef32_pk_fp8_f32 v186, v200, v201, s36
	v_pk_add_f32 v[188:189], v[74:75], v[188:189]
	v_pk_add_f32 v[190:191], v[76:77], v[190:191]
	v_cvt_scalef32_pk_fp8_f32 v187, v202, v203, s36
	v_cvt_scalef32_pk_fp8_f32 v186, v198, v199, s36 op_sel:[0,0,0,1]
	v_pk_add_f32 v[192:193], v[78:79], v[188:189]
	v_pk_add_f32 v[190:191], v[80:81], v[190:191]
	v_mfma_f32_32x32x64_f8f6f4 v[2:17], v[154:161], v[130:137], v[2:17]
	s_nop 0
	s_nop 0
	s_nop 0
	s_nop 0
	s_nop 0
	s_nop 0
	s_mulk_i32 s51, 0x2800
	v_cvt_scalef32_pk_fp8_f32 v188, v194, v195, s36
	v_cvt_scalef32_pk_fp8_f32 v189, v226, v227, s36
	v_cvt_scalef32_pk_fp8_f32 v154, v66, v67, s36
	v_cvt_scalef32_pk_fp8_f32 v155, v70, v71, s36
	v_cvt_scalef32_pk_fp8_f32 v156, v74, v75, s36
	v_cvt_scalef32_pk_fp8_f32 v157, v78, v79, s36
	v_cvt_scalef32_pk_fp8_f32 v187, v196, v197, s36 op_sel:[0,0,0,1]
	v_add_u32_e32 v234, s51, v219
	v_cvt_scalef32_pk_fp8_f32 v188, v224, v225, s36 op_sel:[0,0,0,1]
	v_cvt_scalef32_pk_fp8_f32 v189, v228, v229, s36 op_sel:[0,0,0,1]
	v_cvt_scalef32_pk_fp8_f32 v154, v68, v69, s36 op_sel:[0,0,0,1]
	v_cvt_scalef32_pk_fp8_f32 v155, v72, v73, s36 op_sel:[0,0,0,1]
	v_cvt_scalef32_pk_fp8_f32 v156, v76, v77, s36 op_sel:[0,0,0,1]
	v_cvt_scalef32_pk_fp8_f32 v157, v80, v81, s36 op_sel:[0,0,0,1]
	v_exp_f32_e32 v98, v98
	v_exp_f32_e32 v99, v99
	v_mfma_f32_32x32x64_f8f6f4 v[34:49], v[146:153], v[138:145], v[34:49]
	v_exp_f32_e32 v100, v100
	v_exp_f32_e32 v101, v101
	v_exp_f32_e32 v102, v102
	v_exp_f32_e32 v103, v103
	v_exp_f32_e32 v104, v104
	v_exp_f32_e32 v105, v105
	v_exp_f32_e32 v106, v106
	v_exp_f32_e32 v107, v107
	v_exp_f32_e32 v108, v108
	v_exp_f32_e32 v109, v109
	v_exp_f32_e32 v110, v110
	v_exp_f32_e32 v111, v111
	v_exp_f32_e32 v112, v112
	v_exp_f32_e32 v113, v113
	ds_read_b128 v[194:197], v234
	ds_read_b128 v[198:201], v234 offset:16
	v_pk_add_f32 v[66:67], v[232:233], v[98:99]
	v_pk_add_f32 v[68:69], v[230:231], v[100:101]
	v_pk_add_f32 v[66:67], v[102:103], v[66:67]
	v_pk_add_f32 v[68:69], v[104:105], v[68:69]
	v_pk_add_f32 v[66:67], v[106:107], v[66:67]
	v_pk_add_f32 v[68:69], v[108:109], v[68:69]
	v_pk_add_f32 v[140:141], v[110:111], v[66:67]
	v_pk_add_f32 v[138:139], v[112:113], v[68:69]
	v_mfma_f32_32x32x64_f8f6f4 v[18:33], v[146:153], v[130:137], v[18:33]
	v_exp_f32_e32 v82, v82
	v_exp_f32_e32 v83, v83
	v_exp_f32_e32 v84, v84
	v_exp_f32_e32 v85, v85
	v_exp_f32_e32 v86, v86
	v_exp_f32_e32 v87, v87
	v_exp_f32_e32 v88, v88
	v_exp_f32_e32 v89, v89
	v_exp_f32_e32 v90, v90
	v_exp_f32_e32 v91, v91
	v_exp_f32_e32 v92, v92
	v_exp_f32_e32 v93, v93
	v_exp_f32_e32 v94, v94
	v_exp_f32_e32 v95, v95
	v_exp_f32_e32 v96, v96
	v_exp_f32_e32 v97, v97
	v_pk_add_f32 v[66:67], v[192:193], v[82:83]
	v_pk_add_f32 v[68:69], v[190:191], v[84:85]
	v_pk_add_f32 v[66:67], v[86:87], v[66:67]
	v_pk_add_f32 v[68:69], v[88:89], v[68:69]
	v_pk_add_f32 v[130:131], v[90:91], v[66:67]
	v_pk_add_f32 v[132:133], v[92:93], v[68:69]
	s_waitcnt lgkmcnt(0)
; DI KParamsPtr kparams() { KParamsPtr p = (KParamsPtr)__builtin_amdgcn_kernarg_segment_ptr(); asm volatile("" : "+s"(p)); return p; }
; DI f32x16 mfma8(v8i a, v8i b, f32x16 c) { return __builtin_amdgcn_mfma_scale_f32_32x32x64_f8f6f4(a, b, c, 0, 0, 0, 0, 0, 0); }
; DI void attn_unit_a8(unsigned char* lds, const AttnArgs& a) {
;     ...
;     auto w_decode = [&](int j, const float*& src, unsigned char*& dst, int& ld, int& n0, int& k0, bool& gu) __attribute__((always_inline)) {
;         const int g = (j >> 2) * 512 + a.wl, e = g / 96, rr = g - e * 96; KParamsPtr kp = kparams();
;         if (rr < 64) { src = kp->w_gu + ((size_t)a.wli * NE + e) * (1024 * 2048); dst = kp->ws + WS_WGU + (size_t)a.wli * SZ_WGU + (size_t)e * 2048 * 1024; ld = 2048; n0 = (rr & 7) * 256; k0 = ((rr >> 3) * 4 + (j & 3)) * 32; gu = true; }
;         else { const int q = rr - 64; src = kp->w_dn + ((size_t)a.wli * NE + e) * (1024 * 1024); dst = kp->ws + WS_WDN + (size_t)a.wli * SZ_WDN + (size_t)e * 1024 * 1024; ld = 1024; n0 = (q & 3) * 256; k0 = ((q >> 2) * 4 + (j & 3)) * 32; gu = false; } };
; DI void attn_unit_d8(unsigned char* lds, const AttnArgs& a) {
;     ...
;     auto tile = [&](const unsigned char* Kb, const unsigned char* Kn, v8i& Pa, v8i& Pb, v8i& v0, v8i& v1, const v8i& Qa, const v8i& Qb, const v8i& w0, const v8i& w1) __attribute__((always_inline)) {
;         qk(Kb, 1, s1a, s1b);
;         v0 = rd32(Kb + voff); v1 = rd32(Kb + voff + 32 * A8_PITCH);
;         o0[0] = mfma8(w0, Qa, o0[0]); o1[0] = mfma8(w0, Qb, o1[0]); o0[1] = mfma8(w1, Qa, o0[1]); o1[1] = mfma8(w1, Qb, o1[1]);
;         expsum(s0a, l0); expsum(s0b, l1); pack4(s0a, Pa, 0); pack4(s0b, Pb, 0);
;         qk(Kn, 0, s0a, s0b);
;         expsum(s1a, l0); expsum(s1b, l1); pack4(s1a, Pa, 4); pack4(s1b, Pb, 4);
; #pragma unroll
;         for (int i = 0; i < 8; ++i) { __builtin_amdgcn_sched_group_barrier(0x008, 1, 0); __builtin_amdgcn_sched_group_barrier(0x402, 22, 0); }
;     };
	v_mfma_f32_32x32x64_f8f6f4 v[66:81], v[194:201], v[114:121], 0
	s_nop 0
	s_nop 0
	s_nop 0
	s_nop 0
	s_nop 0
	s_nop 0
	s_nop 0
	v_cvt_scalef32_pk_fp8_f32 v190, v98, v99, s36
	v_cvt_scalef32_pk_fp8_f32 v191, v102, v103, s36
	v_cvt_scalef32_pk_fp8_f32 v192, v106, v107, s36
	v_cvt_scalef32_pk_fp8_f32 v193, v110, v111, s36
	v_cvt_scalef32_pk_fp8_f32 v158, v82, v83, s36
	v_cvt_scalef32_pk_fp8_f32 v159, v86, v87, s36
	v_pk_add_f32 v[142:143], v[96:97], v[132:133]
	v_pk_add_f32 v[144:145], v[94:95], v[130:131]
	v_cvt_scalef32_pk_fp8_f32 v160, v90, v91, s36
	v_cvt_scalef32_pk_fp8_f32 v190, v100, v101, s36 op_sel:[0,0,0,1]
	v_cvt_scalef32_pk_fp8_f32 v191, v104, v105, s36 op_sel:[0,0,0,1]
	v_cvt_scalef32_pk_fp8_f32 v192, v108, v109, s36 op_sel:[0,0,0,1]
	v_cvt_scalef32_pk_fp8_f32 v193, v112, v113, s36 op_sel:[0,0,0,1]
	v_cvt_scalef32_pk_fp8_f32 v158, v84, v85, s36 op_sel:[0,0,0,1]
	v_cvt_scalef32_pk_fp8_f32 v159, v88, v89, s36 op_sel:[0,0,0,1]
	v_mfma_f32_32x32x64_f8f6f4 v[98:113], v[194:201], v[122:129], 0
	global_load_dwordx2 v[194:195], v[220:221], off
	global_load_dwordx2 v[196:197], v[222:223], off
	ds_read_b128 v[130:133], v234 offset:2560
	ds_read_b128 v[134:137], v234 offset:2576
	v_exp_f32_e32 v146, v66
	s_lshr_b32 s73, s61, 2
	v_exp_f32_e32 v147, v67
	s_add_i32 s73, s73, 3
	s_mulk_i32 s52, 0x2800
	s_nop 0
	s_add_i32 s8, s52, 0
	v_cvt_scalef32_pk_fp8_f32 v161, v94, v95, s36
	v_add_u32_e32 v224, s8, v183
	v_cvt_scalef32_pk_fp8_f32 v160, v92, v93, s36 op_sel:[0,0,0,1]
	v_cvt_scalef32_pk_fp8_f32 v161, v96, v97, s36 op_sel:[0,0,0,1]
	v_exp_f32_e32 v148, v68
	s_lshl_b32 s73, s73, 9
	v_exp_f32_e32 v149, v69
	s_add_i32 s73, s73, s46
	v_exp_f32_e32 v150, v70
	s_mul_i32 s75, s73, 0xaaab
	v_exp_f32_e32 v151, v71
	s_lshr_b32 s75, s75, 22
	v_exp_f32_e32 v152, v72
	s_mul_i32 s76, s75, 0x60
	v_exp_f32_e32 v153, v73
	s_sub_i32 s76, s73, s76
	v_exp_f32_e32 v198, v74
	s_lshr_b32 s77, s76, 6
	v_exp_f32_e32 v199, v75
	s_lshl_b32 s78, s77, 6
	v_exp_f32_e32 v200, v76
	s_sub_i32 s76, s76, s78
	v_exp_f32_e32 v201, v77
	s_sub_i32 s78, 3, s77
	v_exp_f32_e32 v202, v78
	s_lshr_b32 s79, s76, s78
	v_exp_f32_e32 v203, v79
	s_lshl_b32 s79, s79, 2
	v_exp_f32_e32 v220, v80
	s_and_b32 s81, s61, 3
	v_exp_f32_e32 v221, v81
	s_add_i32 s79, s79, s81
	v_pk_add_f32 v[66:67], v[140:141], v[146:147]
	s_waitcnt lgkmcnt(0)
	v_mfma_f32_32x32x64_f8f6f4 v[82:97], v[130:137], v[114:121], 0
	v_add_f32_e64 v68, v138, v148
	v_add_f32_e64 v69, v139, v149
	v_add_f32_e64 v66, v150, v66
	v_add_f32_e64 v67, v151, v67
	v_add_f32_e64 v68, v152, v68
	v_add_f32_e64 v69, v153, v69
	v_add_f32_e64 v138, v198, v66
	v_add_f32_e64 v139, v199, v67
	v_add_f32_e64 v140, v200, v68
	v_add_f32_e64 v141, v201, v69
	v_exp_f32_e32 v98, v98
	s_lshl_b32 s79, s79, 5
	v_exp_f32_e32 v99, v99
	s_lshl_b32 s81, s63, 2
	v_exp_f32_e32 v100, v100
	s_add_i32 s81, s81, s79
	v_exp_f32_e32 v101, v101
	s_sub_i32 s78, 13, s77
	v_exp_f32_e32 v102, v102
	s_lshl_b32 s81, s81, s78
	v_exp_f32_e32 v103, v103
	s_lshr_b32 s78, 7, s77
	v_exp_f32_e32 v104, v104
	s_and_b32 s78, s76, s78
	v_exp_f32_e32 v105, v105
	s_lshl_b32 s72, s78, 10
	v_exp_f32_e32 v106, v106
	s_add_i32 s81, s81, s72
	v_exp_f32_e32 v107, v107
	s_add_i32 s72, s75, 32
	v_exp_f32_e32 v108, v108
	s_sub_i32 s80, 23, s77
	v_exp_f32_e32 v109, v109
	s_lshl_b32 s72, s72, s80
	v_exp_f32_e32 v110, v110
	s_add_i32 s81, s81, s72
	v_exp_f32_e32 v111, v111
	s_cmp_eq_u32 s77, 0
	s_cselect_b64 s[84:85], s[66:67], s[68:69]
	v_exp_f32_e32 v112, v112
	s_add_u32 s84, s84, s81
	s_addc_u32 s85, s85, 0
	v_exp_f32_e32 v113, v113
	s_lshr_b32 s80, 0x2000, s77
	v_exp_f32_e32 v82, v82
	s_and_b32 s72, s78, 3
	v_mfma_f32_32x32x64_f8f6f4 v[66:81], v[130:137], v[122:129], 0
	v_add_f32_e64 v130, v144, v98
	v_add_f32_e64 v131, v145, v99
	v_add_f32_e64 v132, v142, v100
	v_add_f32_e64 v133, v143, v101
	v_add_f32_e64 v142, v102, v130
	v_add_f32_e64 v143, v103, v131
	v_add_f32_e64 v132, v104, v132
	v_add_f32_e64 v133, v105, v133
	v_add_f32_e64 v134, v220, v140
	v_add_f32_e64 v135, v221, v141
	v_add_f32_e64 v136, v202, v138
	v_add_f32_e64 v137, v203, v139
	s_nop 0
	s_nop 0
	s_nop 0
	s_nop 0
	s_nop 0
	s_nop 0
	v_pk_add_f32 v[142:143], v[106:107], v[142:143]
	v_pk_add_f32 v[132:133], v[108:109], v[132:133]
	v_cvt_scalef32_pk_fp8_f32 v138, v146, v147, s36
	v_cvt_scalef32_pk_fp8_f32 v139, v150, v151, s36
	v_cvt_scalef32_pk_fp8_f32 v140, v198, v199, s36
	v_cvt_scalef32_pk_fp8_f32 v141, v202, v203, s36
	v_cvt_scalef32_pk_fp8_f32 v130, v98, v99, s36
	v_cvt_scalef32_pk_fp8_f32 v131, v102, v103, s36
	v_pk_add_f32 v[146:147], v[112:113], v[132:133]
	v_pk_add_f32 v[150:151], v[110:111], v[142:143]
	v_mfma_f32_32x32x64_f8f6f4 v[50:65], v[170:177], v[186:193], v[50:65]
	v_exp_f32_e32 v83, v83
	s_lshl_b32 s72, s72, 19
	v_exp_f32_e32 v84, v84
	s_lshr_b32 s81, s78, 2
	v_exp_f32_e32 v85, v85
	s_lshl_b32 s81, s81, 17
	v_add_u32_e32 v102, s50, v219
	v_exp_f32_e32 v86, v86
	s_add_i32 s72, s72, s81
	v_exp_f32_e32 v87, v87
	s_lshl_b32 s81, s78, 18
	v_exp_f32_e32 v88, v88
	s_cmp_eq_u32 s77, 0
	s_cselect_b32 s72, s72, s81
; DI void attn_unit_a8(unsigned char* lds, const AttnArgs& a) {
;     ...
;     auto w_cvt = [&]() __attribute__((always_inline)) { unsigned char* t8 = lds + AT_WT + wn4 * WPITCH + 4 * wid;
; #pragma unroll
;         for (int j = 0; j < 4; ++j) *(unsigned*)(t8 + j * WPITCH) = pk4_fp8_mul64(wq[0][j], wq[1][j], wq[2][j], wq[3][j]); };
;     const int wcol = tid >> 1, whalf = tid & 1;
;     const unsigned wper_gu = (unsigned)((wcol >> 7) * 256 + (wcol & 96) + invperm32(wcol & 31)) * 1024u + 16u * whalf;
;     const unsigned wper_dn = (unsigned)fwd_lane16(wcol) * 1024u + 16u * whalf;
;     auto w_store = [&](int j) __attribute__((always_inline)) { const float* src; unsigned char* dst; int ld, n0, k0; bool gu; w_decode(j, src, dst, ld, n0, k0, gu);
;         const int nb = n0 >> 8; const unsigned uni = (unsigned)(gu ? (nb & 3) * 512 + (nb >> 2) * 128 : nb * 256) * 1024u + (unsigned)k0;
; DI void attn_unit_d8(unsigned char* lds, const AttnArgs& a) {
;     ...
;     auto tile = [&](const unsigned char* Kb, const unsigned char* Kn, v8i& Pa, v8i& Pb, v8i& v0, v8i& v1, const v8i& Qa, const v8i& Qb, const v8i& w0, const v8i& w1) __attribute__((always_inline)) {
;         qk(Kb, 1, s1a, s1b);
;         v0 = rd32(Kb + voff); v1 = rd32(Kb + voff + 32 * A8_PITCH);
;         o0[0] = mfma8(w0, Qa, o0[0]); o1[0] = mfma8(w0, Qb, o1[0]); o0[1] = mfma8(w1, Qa, o0[1]); o1[1] = mfma8(w1, Qb, o1[1]);
;         expsum(s0a, l0); expsum(s0b, l1); pack4(s0a, Pa, 0); pack4(s0b, Pb, 0);
;         qk(Kn, 0, s0a, s0b);
;         expsum(s1a, l0); expsum(s1b, l1); pack4(s1a, Pa, 4); pack4(s1b, Pb, 4);
; #pragma unroll
;         for (int i = 0; i < 8; ++i) { __builtin_amdgcn_sched_group_barrier(0x008, 1, 0); __builtin_amdgcn_sched_group_barrier(0x402, 22, 0); }
;     };
;     for (int t = a.t0; t < a.t1; t += 2) {
;         const int s1 = sb + 1 >= 5 ? sb - 4 : sb + 1, s2 = sb + 2 >= 5 ? sb - 3 : sb + 2, s3 = sb + 3 >= 5 ? sb - 2 : sb + 3, s4 = sb + 4 >= 5 ? sb - 1 : sb + 4;
;         { const int ta = t + 3, tb = t + 4; gload(ta < a.t1 ? ta : a.t1 - 1, kreg0, vreg0); gload(tb < a.t1 ? tb : a.t1 - 1, kreg1, vreg1); }
;         tile(lds + sb * D8_SLOT, lds + s1 * D8_SLOT, PaX, PbX, vX0, vX1, PaY, PbY, vY0, vY1);
;         tile(lds + s1 * D8_SLOT, lds + s2 * D8_SLOT, PaY, PbY, vY0, vY1, PaX, PbX, vX0, vX1);
;         lstore(s3, kreg0, vreg0); lstore(s4, kreg1, vreg1);
	v_exp_f32_e32 v89, v89
	s_mul_i32 s81, s77, 0xc000000
	v_cvt_scalef32_pk_fp8_f32 v130, v100, v101, s36 op_sel:[0,0,0,1]
	v_cvt_scalef32_pk_fp8_f32 v131, v104, v105, s36 op_sel:[0,0,0,1]
	v_exp_f32_e32 v90, v90
	s_add_i32 s81, s81, 0x9094000
	v_exp_f32_e32 v91, v91
	s_add_i32 s72, s72, s79
	v_exp_f32_e32 v92, v92
	s_sub_i32 s73, 21, s77
	v_exp_f32_e32 v93, v93
	s_lshl_b32 s73, s75, s73
	ds_read_b128 v[98:101], v102
	ds_read_b128 v[102:105], v102 offset:16
	s_nop 0
	v_cvt_scalef32_pk_fp8_f32 v138, v148, v149, s36 op_sel:[0,0,0,1]
	v_cvt_scalef32_pk_fp8_f32 v139, v152, v153, s36 op_sel:[0,0,0,1]
	v_cvt_scalef32_pk_fp8_f32 v140, v200, v201, s36 op_sel:[0,0,0,1]
	v_cvt_scalef32_pk_fp8_f32 v141, v220, v221, s36 op_sel:[0,0,0,1]
	s_nop 0
	v_exp_f32_e32 v94, v94
	s_add_i32 s72, s72, s73
	v_exp_f32_e32 v95, v95
	s_add_u32 s72, s72, s81
	v_mfma_f32_32x32x64_f8f6f4 v[2:17], v[170:177], v[154:161], v[2:17]
	v_exp_f32_e32 v148, v96
	s_or_b32 s79, s72, s77
	v_cvt_scalef32_pk_fp8_f32 v132, v106, v107, s36
	v_exp_f32_e32 v149, v97
	v_pk_add_f32 v[96:97], v[136:137], v[82:83]
	v_pk_add_f32 v[106:107], v[134:135], v[84:85]
	v_exp_f32_e32 v66, v66
	v_exp_f32_e32 v67, v67
	v_exp_f32_e32 v68, v68
	v_exp_f32_e32 v69, v69
	v_cvt_scalef32_pk_fp8_f32 v133, v110, v111, s36
	v_pk_add_f32 v[106:107], v[88:89], v[106:107]
	v_pk_add_f32 v[96:97], v[86:87], v[96:97]
	v_exp_f32_e32 v70, v70
	v_exp_f32_e32 v71, v71
	v_exp_f32_e32 v72, v72
	v_exp_f32_e32 v73, v73
	v_cvt_scalef32_pk_fp8_f32 v132, v108, v109, s36 op_sel:[0,0,0,1]
	v_cvt_scalef32_pk_fp8_f32 v133, v112, v113, s36 op_sel:[0,0,0,1]
	v_pk_add_f32 v[96:97], v[90:91], v[96:97]
	v_pk_add_f32 v[106:107], v[92:93], v[106:107]
	v_exp_f32_e32 v74, v74
	v_exp_f32_e32 v75, v75
	v_mfma_f32_32x32x64_f8f6f4 v[34:49], v[162:169], v[186:193], v[34:49]
	v_exp_f32_e32 v76, v76
	v_exp_f32_e32 v77, v77
	v_exp_f32_e32 v78, v78
	v_exp_f32_e32 v79, v79
	s_nop 0
	v_exp_f32_e32 v80, v80
	v_exp_f32_e32 v81, v81
	s_nop 0
	s_nop 0
	v_cvt_scalef32_pk_fp8_f32 v142, v82, v83, s36
	s_nop 0
	v_cvt_scalef32_pk_fp8_f32 v143, v86, v87, s36
	v_cvt_scalef32_pk_fp8_f32 v144, v90, v91, s36
	v_cvt_scalef32_pk_fp8_f32 v142, v84, v85, s36 op_sel:[0,0,0,1]
	v_pk_add_f32 v[82:83], v[150:151], v[66:67]
	v_pk_add_f32 v[84:85], v[146:147], v[68:69]
	s_mulk_i32 s53, 0x2800
	v_pk_add_f32 v[186:187], v[148:149], v[106:107]
	v_pk_add_f32 v[188:189], v[94:95], v[96:97]
	v_cvt_scalef32_pk_fp8_f32 v145, v94, v95, s36
	v_cvt_scalef32_pk_fp8_f32 v143, v88, v89, s36 op_sel:[0,0,0,1]
	v_cvt_scalef32_pk_fp8_f32 v144, v92, v93, s36 op_sel:[0,0,0,1]
	v_pk_add_f32 v[84:85], v[72:73], v[84:85]
	v_mfma_f32_32x32x64_f8f6f4 v[18:33], v[162:169], v[154:161], v[18:33]
	v_add_f32_e64 v82, v70, v82
	v_add_f32_e64 v83, v71, v83
	s_nop 0
	s_nop 0
	s_nop 0
	s_nop 0
	s_add_i32 s51, s53, 0
	v_add_f32_e64 v82, v74, v82
	v_add_f32_e64 v83, v75, v83
	v_add_f32_e64 v84, v76, v84
	v_add_f32_e64 v85, v77, v85
	v_cvt_scalef32_pk_fp8_f32 v134, v66, v67, s36
	v_cvt_scalef32_pk_fp8_f32 v135, v70, v71, s36
	v_cvt_scalef32_pk_fp8_f32 v136, v74, v75, s36
	v_cvt_scalef32_pk_fp8_f32 v137, v78, v79, s36
	v_pk_add_f32 v[190:191], v[80:81], v[84:85]
	v_pk_add_f32 v[192:193], v[78:79], v[82:83]
	v_add_u32_e32 v106, s8, v218
	v_add_u32_e32 v107, s51, v183
	v_cvt_scalef32_pk_fp8_f32 v145, v148, v149, s36 op_sel:[0,0,0,1]
	v_cvt_scalef32_pk_fp8_f32 v134, v68, v69, s36 op_sel:[0,0,0,1]
	v_cvt_scalef32_pk_fp8_f32 v135, v72, v73, s36 op_sel:[0,0,0,1]
	v_cvt_scalef32_pk_fp8_f32 v136, v76, v77, s36 op_sel:[0,0,0,1]
	v_cvt_scalef32_pk_fp8_f32 v137, v80, v81, s36 op_sel:[0,0,0,1]
	s_waitcnt lgkmcnt(0)
	v_mfma_f32_32x32x64_f8f6f4 v[82:97], v[98:105], v[114:121], 0
	ds_read_b128 v[154:157], v234 offset:5120
	ds_read_b128 v[158:161], v234 offset:5136
	ds_read_b128 v[146:149], v234 offset:7680
	ds_read_b128 v[150:153], v234 offset:7696
	s_cmpk_gt_i32 s46, 0x1ff
	s_cbranch_scc1 .Lmy_rd1_ldum
	s_add_i32 s72, s61, -1
	s_cmp_lt_u32 s72, 12
	s_cbranch_scc0 .Lmy_rd1_noc
	s_waitcnt vmcnt(4)
	v_cvt_scalef32_pk_fp8_f32 v236, v236, v240, s62
	v_cvt_scalef32_pk_fp8_f32 v237, v237, v241, s62
	v_cvt_scalef32_pk_fp8_f32 v238, v238, v242, s62
	v_cvt_scalef32_pk_fp8_f32 v239, v239, v243, s62
	v_cvt_scalef32_pk_fp8_f32 v236, v244, v248, s62 op_sel:[0,0,0,1]
	v_cvt_scalef32_pk_fp8_f32 v237, v245, v249, s62 op_sel:[0,0,0,1]
	v_cvt_scalef32_pk_fp8_f32 v238, v246, v250, s62 op_sel:[0,0,0,1]
	v_cvt_scalef32_pk_fp8_f32 v239, v247, v251, s62 op_sel:[0,0,0,1]
	ds_write_b32 v252, v236
	ds_write_b32 v252, v237 offset:36
	ds_write_b32 v252, v238 offset:72
	ds_write_b32 v252, v239 offset:108
.Lmy_rd1_noc:
	ds_read2_b32 v[244:245], v253 offset1:1
	ds_read2_b32 v[246:247], v253 offset0:2 offset1:3
	s_cmpk_gt_i32 s46, 0x1ff
	s_cbranch_scc1 .Lmy_rd1_sdum
	s_add_i32 s72, s61, -2
	s_cmp_lt_u32 s72, 12
	s_cbranch_scc0 .Lmy_rd1_sdum
	s_andn2_b32 s73, s65, 1
	s_add_u32 s82, s70, s73
	s_addc_u32 s83, s71, 0
	s_bitcmp1_b32 s65, 0
	s_cbranch_scc1 .Lmy_rd1_sdn
	s_waitcnt lgkmcnt(0)
	global_store_dwordx4 v254, v[244:247], s[82:83]
	s_branch .Lmy_rd1_sdone

; DI void attn_unit_a8(unsigned char* lds, const AttnArgs& a) {
;     ...
;     auto w_issue = [&](int j) __attribute__((always_inline)) { const float* src; unsigned char* dst; int ld, n0, k0; bool gu; w_decode(j, src, dst, ld, n0, k0, gu);
;         const float* p = src + (size_t)(k0 + 4 * wid) * ld + n0 + wn4;
;         wq[0] = __builtin_nontemporal_load((const f32x4*)p); wq[1] = __builtin_nontemporal_load((const f32x4*)(p + ld));
;         wq[2] = __builtin_nontemporal_load((const f32x4*)(p + (size_t)2 * ld)); wq[3] = __builtin_nontemporal_load((const f32x4*)(p + (size_t)3 * ld)); };
.Lmy_rd1_sdone:
	s_cmpk_gt_i32 s46, 0x1ff
	s_cbranch_scc1 .Lmy_rd1_ld0
	s_cmp_lt_u32 s61, 12
	s_cbranch_scc1 .Lmy_rd1_lgo

; DI void attn_unit_a8(unsigned char* lds, const AttnArgs& a) {
;     ...
;     auto w_cvt = [&]() __attribute__((always_inline)) { unsigned char* t8 = lds + AT_WT + wn4 * WPITCH + 4 * wid;
; #pragma unroll
;         for (int j = 0; j < 4; ++j) *(unsigned*)(t8 + j * WPITCH) = pk4_fp8_mul64(wq[0][j], wq[1][j], wq[2][j], wq[3][j]); };
;     const int wcol = tid >> 1, whalf = tid & 1;
;     const unsigned wper_gu = (unsigned)((wcol >> 7) * 256 + (wcol & 96) + invperm32(wcol & 31)) * 1024u + 16u * whalf;
;     const unsigned wper_dn = (unsigned)fwd_lane16(wcol) * 1024u + 16u * whalf;
;     auto w_store = [&](int j) __attribute__((always_inline)) { const float* src; unsigned char* dst; int ld, n0, k0; bool gu; w_decode(j, src, dst, ld, n0, k0, gu);
;         const int nb = n0 >> 8; const unsigned uni = (unsigned)(gu ? (nb & 3) * 512 + (nb >> 2) * 128 : nb * 256) * 1024u + (unsigned)k0;
;         const unsigned off = (gu ? wper_gu : wper_dn) + uni;
;         const unsigned* t = (const unsigned*)(lds + AT_WT + wcol * WPITCH + 16 * whalf);
;         *(u32x4*)(dst + off) = (u32x4){t[0], t[1], t[2], t[3]}; };
;     ...
;     auto step = [&](int t, u32x2& kl, u32x2& vl, const u32x2& ks, const u32x2& vs, f32x16& c0, f32x16& c1, f32x16& n0, f32x16& n1, const int hk, const int wj) __attribute__((always_inline)) {
;         const int slot1 = slot == 2 ? 0 : slot + 1, slot2 = slot1 == 2 ? 0 : slot1 + 1;
;         if (hk == 1) { w_cvt(); w_issue(wj + 1 < AT_NWT ? wj + 1 : AT_NWT - 1); }
;         if (hk == 2) w_store(wj);
;         { const int tn = t + 3; gload(tn < a.t1 ? tn : a.t1 - 1, kl, vl); }
;         const unsigned char* Kb = lds + slot * AT_BUFB; const unsigned char* Kn = lds + slot1 * AT_BUFB;
;         const v8i k0 = kread(Kn, 0), k1 = kread(Kn, 1), v0 = vread(Kb, 0), v1 = vread(Kb, 1);
;         n0 = mfma8(k0, qf8, cinit); n1 = mfma8(k1, qf8, cinit);
;         expsum(c0); expsum(c1);
;         const v8i P = pack8(c0, c1);
;         o0[0] = mfma8(v0, P, o0[0]); o0[1] = mfma8(v1, P, o0[1]);
;         lstore(slot2, ks, vs);
;         __syncthreads();
;         slot = slot1;
;     };
;     {
;         int t = a.t0;
;         if (wrider)
;             for (int j = 0; j < AT_NWT; ++j, t += 2) { step(t, kregB, vregB, kregA, vregA, sx0, sx1, sy0, sy1, 1, j); step(t + 1, kregA, vregA, kregB, vregB, sy0, sy1, sx0, sx1, 2, j); }
.LBB0_1922:
	s_lshl_b32 s8, s18, 1
	s_waitcnt lgkmcnt(0)
	s_lshr_b32 s16, s18, 3
	s_and_b32 s8, s8, 0x600
	s_and_b32 s16, s16, 0x80
	s_or_b32 s8, s8, s16
	s_and_b64 s[14:15], s[14:15], exec
	v_pk_add_f32 v[54:55], v[164:165], v[108:109]
	s_cselect_b32 s8, s8, s18
	s_and_b32 s14, s50, 3
	v_pk_add_f32 v[54:55], v[154:155], v[54:55]
	s_add_i32 s14, s52, s14
	v_pk_add_f32 v[54:55], v[158:159], v[54:55]
	s_lshl_b32 s14, s14, 5
	s_lshl_b32 s8, s8, 10
	v_pk_add_f32 v[56:57], v[160:161], v[110:111]
	v_pk_add_f32 v[46:47], v[46:47], v[54:55]
	s_add_i32 s14, s8, s14
	s_add_i32 s51, s51, 1
	v_pk_add_f32 v[56:57], v[162:163], v[56:57]
	v_pk_add_f32 v[46:47], v[50:51], v[46:47]
	s_and_b64 s[12:13], s[12:13], exec
	v_pk_add_f32 v[56:57], v[152:153], v[56:57]
	v_pk_add_f32 v[40:41], v[40:41], v[46:47]
	s_cselect_b32 s18, 0, s51
	v_pk_add_f32 v[56:57], v[156:157], v[56:57]
	v_pk_add_f32 v[50:51], v[42:43], v[40:41]
	s_mul_i32 s8, s18, 0x4680
	v_pk_add_f32 v[44:45], v[44:45], v[56:57]
	v_add_u32_e32 v58, s8, v169
	v_pk_add_f32 v[110:111], v[34:35], v[50:51]
	v_add_u32_e32 v34, 0xd800, v175
	v_pk_add_f32 v[48:49], v[48:49], v[44:45]
	ds_read_b128 v[40:43], v58
	ds_read_b128 v[44:47], v58 offset:16
	v_add_u32_e32 v35, 0xd808, v175
	ds_read2_b32 v[54:55], v34 offset1:1
	ds_read2_b32 v[56:57], v35 offset1:1
	v_add_u32_e32 v50, v52, v170
	v_lshl_or_b32 v50, v50, 10, v172
	v_add_u32_e32 v50, s14, v50
	v_exp_f32_e32 v82, v82
	s_waitcnt lgkmcnt(0)
	global_store_dwordx4 v50, v[54:57], s[10:11]
	ds_read_b128 v[50:53], v58 offset:2560
	ds_read_b128 v[54:57], v58 offset:2576
	v_add_co_u32_e32 v58, vcc, s70, v148
	v_exp_f32_e32 v83, v83
	s_nop 0
	v_addc_co_u32_e32 v59, vcc, 0, v149, vcc
	global_load_dwordx2 v[136:137], v[58:59], off
	global_load_dwordx2 v[138:139], v[150:151], off offset:256
	v_exp_f32_e32 v86, v86
	v_exp_f32_e32 v87, v87
	v_exp_f32_e32 v90, v90
	v_exp_f32_e32 v91, v91
	v_exp_f32_e32 v94, v94
	v_exp_f32_e32 v95, v95
	v_exp_f32_e32 v164, v66
	v_exp_f32_e32 v165, v67
	v_exp_f32_e32 v178, v70
	v_exp_f32_e32 v179, v71
	v_exp_f32_e32 v74, v74
	v_exp_f32_e32 v75, v75
	v_exp_f32_e32 v78, v78
	v_exp_f32_e32 v79, v79
	ds_read_b128 v[148:151], v176 offset:5120
	ds_read_b128 v[152:155], v176 offset:5136
	ds_read_b128 v[156:159], v176 offset:7680
	ds_read_b128 v[160:163], v176 offset:7696
	v_exp_f32_e32 v84, v84
	v_exp_f32_e32 v85, v85
	v_exp_f32_e32 v88, v88
	v_exp_f32_e32 v89, v89
	v_exp_f32_e32 v92, v92
	v_exp_f32_e32 v93, v93
	v_exp_f32_e32 v96, v96
	v_exp_f32_e32 v97, v97
	v_exp_f32_e32 v176, v68
	v_exp_f32_e32 v177, v69
	v_exp_f32_e32 v180, v72
	v_exp_f32_e32 v181, v73
	v_exp_f32_e32 v76, v76
	v_exp_f32_e32 v77, v77
	v_exp_f32_e32 v80, v80
	v_exp_f32_e32 v81, v81
	s_nop 0
	s_nop 0
	s_nop 0
	s_nop 0
	s_nop 0
	s_nop 0
	s_nop 0
	s_nop 0
	v_cvt_scalef32_pk_fp8_f32 v66, v82, v83, s69
	v_cvt_scalef32_pk_fp8_f32 v70, v164, v165, s69
	v_cvt_scalef32_pk_fp8_f32 v67, v86, v87, s69
	v_cvt_scalef32_pk_fp8_f32 v71, v178, v179, s69
	v_cvt_scalef32_pk_fp8_f32 v68, v90, v91, s69
	v_cvt_scalef32_pk_fp8_f32 v72, v74, v75, s69
	v_cvt_scalef32_pk_fp8_f32 v69, v94, v95, s69
	v_cvt_scalef32_pk_fp8_f32 v73, v78, v79, s69
	v_pk_add_f32 v[36:37], v[36:37], v[48:49]
	v_cvt_scalef32_pk_fp8_f32 v66, v84, v85, s69 op_sel:[0,0,0,1]
	v_cvt_scalef32_pk_fp8_f32 v70, v176, v177, s69 op_sel:[0,0,0,1]
	v_cvt_scalef32_pk_fp8_f32 v67, v88, v89, s69 op_sel:[0,0,0,1]
	v_cvt_scalef32_pk_fp8_f32 v71, v180, v181, s69 op_sel:[0,0,0,1]
	v_cvt_scalef32_pk_fp8_f32 v68, v92, v93, s69 op_sel:[0,0,0,1]
	v_cvt_scalef32_pk_fp8_f32 v72, v76, v77, s69 op_sel:[0,0,0,1]
	v_cvt_scalef32_pk_fp8_f32 v69, v96, v97, s69 op_sel:[0,0,0,1]
	v_cvt_scalef32_pk_fp8_f32 v73, v80, v81, s69 op_sel:[0,0,0,1]
	v_pk_add_f32 v[108:109], v[38:39], v[36:37]
	v_mfma_f32_32x32x64_f8f6f4 v[34:49], v[40:47], v[98:105], 0
	v_add_f32_e64 v110, v110, v82
	v_add_f32_e64 v111, v111, v83
	v_add_f32_e64 v82, v108, v84
	v_add_f32_e64 v83, v109, v85
	v_add_f32_e64 v84, v86, v110
	v_add_f32_e64 v85, v87, v111
	v_add_f32_e64 v82, v88, v82
	v_add_f32_e64 v83, v89, v83
	s_addk_i32 s8, 0x4680
	v_add_f32_e64 v84, v90, v84
	v_add_f32_e64 v85, v91, v85
	v_add_f32_e64 v82, v92, v82
	v_add_f32_e64 v83, v93, v83
	s_cmp_lg_u32 s18, 2
	v_pk_add_f32 v[82:83], v[96:97], v[82:83]
	v_pk_add_f32 v[84:85], v[94:95], v[84:85]
	s_cselect_b32 s8, s8, 0
	v_pk_add_f32 v[84:85], v[164:165], v[84:85]
	v_pk_add_f32 v[82:83], v[176:177], v[82:83]
	s_add_i32 s8, s8, 0
	v_pk_add_f32 v[82:83], v[180:181], v[82:83]
	s_waitcnt lgkmcnt(4)
	v_mfma_f32_32x32x64_f8f6f4 v[50:65], v[50:57], v[98:105], 0
	v_add_f32_e64 v84, v178, v84
	v_add_f32_e64 v85, v179, v85
	v_add_f32_e64 v76, v76, v82
	v_add_f32_e64 v77, v77, v83
	v_add_f32_e64 v74, v74, v84
	v_add_f32_e64 v75, v75, v85
	s_add_i32 s50, s50, 1
	s_addk_i32 s23, 0x80
	v_add_f32_e64 v110, v80, v76
	v_add_f32_e64 v111, v81, v77
	v_add_f32_e64 v108, v78, v74
	v_add_f32_e64 v109, v79, v75
	v_lshl_add_u64 v[140:141], v[140:141], 0, s[36:37]
	s_cmp_lg_u32 s50, 12
	v_lshl_add_u64 v[142:143], v[142:143], 0, s[38:39]
	s_waitcnt lgkmcnt(2)
	v_mfma_f32_32x32x64_f8f6f4 v[18:33], v[148:155], v[66:73], v[18:33]
	s_waitcnt lgkmcnt(0)
	v_mfma_f32_32x32x64_f8f6f4 v[2:17], v[156:163], v[66:73], v[2:17]
	v_add_u32_e32 v66, s8, v131
	s_waitcnt vmcnt(4)
	ds_write_b64 v66, v[144:145]
	v_add_u32_e32 v66, s8, v168
	v_add_u32_e32 v66, 0x1400, v66
	s_waitcnt vmcnt(3)
	ds_write2_b32 v66, v146, v147 offset1:8
	s_waitcnt lgkmcnt(0)
	s_barrier
	s_cbranch_scc0 .LBB0_1931
.LBB0_1923:
	s_min_u32 s19, s50, 10
	s_add_i32 s19, s19, 1
	s_lshl_b32 s8, s19, 7
	s_and_b32 s8, s8, 0x1e00
	s_nop 0
	s_nop 0
	s_add_i32 s10, s8, s76
	v_cvt_scalef32_pk_fp8_f32 v66, v116, v112, s66
	v_cvt_scalef32_pk_fp8_f32 v67, v117, v113, s66
	s_mul_hi_u32 s8, s10, 0xaaaaaaab
	v_cvt_scalef32_pk_fp8_f32 v66, v120, v124, s66 op_sel:[0,0,0,1]
	v_cvt_scalef32_pk_fp8_f32 v67, v121, v125, s66 op_sel:[0,0,0,1]
	v_add_u32_e32 v68, 0xd800, v174
	s_lshr_b32 s8, s8, 6
	ds_write2_b32 v68, v66, v67 offset1:9
	s_nop 0
	s_nop 0
	s_mul_i32 s52, s8, 0xffffffa0
	v_cvt_scalef32_pk_fp8_f32 v66, v118, v114, s66
	v_cvt_scalef32_pk_fp8_f32 v67, v119, v115, s66
	s_add_i32 s52, s52, s10
	v_cvt_scalef32_pk_fp8_f32 v66, v122, v126, s66 op_sel:[0,0,0,1]
	v_cvt_scalef32_pk_fp8_f32 v67, v123, v127, s66 op_sel:[0,0,0,1]
	s_mov_b64 s[14:15], s[0:1]
	s_cmp_gt_i32 s52, 63
	s_mov_b64 s[16:17], -1
	ds_write2_b32 v68, v66, v67 offset0:18 offset1:27
	s_cbranch_scc0 .LBB0_1925
	s_load_dwordx2 s[10:11], s[14:15], 0xc0
	s_lshl_b64 s[12:13], s[8:9], 22
	s_mov_b64 s[16:17], 0
	s_waitcnt lgkmcnt(0)
	s_add_u32 s10, s10, s12
	s_addc_u32 s11, s11, s13
	s_add_u32 s10, s10, 0x8000000
	s_addc_u32 s11, s11, 0
	s_and_b32 s12, s52, 0x7ffffffc
	s_sub_i32 s51, s12, 64
